# LSTM layer-2 main loop and fused FC head rewritten by hand with the same schedule as layer 1 (conflict-free LDS layout, 3-deep B prefetch, merged-reciprocal cell update)
# speedup vs baseline: 1.0675x; 1.0172x over previous
_Z6k_lstmILi256ELi10ELb1ELb0EEvPKDF16_S1_S1_PKfPDF16_S1_S1_S1_S3_S3_S3_PfS5_:
	v_lshrrev_b32_e32 v195, 6, v0
	v_and_b32_e32 v205, 15, v0
	v_bfe_u32 v196, v0, 4, 2
	s_cmpk_lt_u32 s2, 0xd1
	s_mov_b64 s[4:5], -1
	s_cbranch_scc0 .LBB6_33
	s_load_dwordx4 s[4:7], s[0:1], 0x10
	s_load_dwordx2 s[8:9], s[0:1], 0x0
	s_load_dwordx2 s[10:11], s[0:1], 0x20
	v_and_b32_e32 v1, 63, v0
	v_lshrrev_b32_e32 v253, 6, v0
	v_mul_u32_u24_e32 v254, 0xc000, v253
	v_lshl_add_u32 v254, v1, 4, v254
	v_lshlrev_b32_e32 v255, 13, v253
	v_lshl_add_u32 v255, v1, 4, v255
	s_waitcnt lgkmcnt(0)
	v_add_u32_e32 v1, 0x0, v254
	global_load_dwordx4 v[2:5], v1, s[4:5] offset:0
	global_load_dwordx4 v[6:9], v1, s[4:5] offset:1024
	global_load_dwordx4 v[10:13], v1, s[4:5] offset:2048
	global_load_dwordx4 v[14:17], v1, s[4:5] offset:3072
	v_add_u32_e32 v1, 0x1000, v254
	global_load_dwordx4 v[18:21], v1, s[4:5] offset:0
	global_load_dwordx4 v[22:25], v1, s[4:5] offset:1024
	global_load_dwordx4 v[26:29], v1, s[4:5] offset:2048
	global_load_dwordx4 v[30:33], v1, s[4:5] offset:3072
	v_add_u32_e32 v1, 0x2000, v254
	global_load_dwordx4 v[34:37], v1, s[4:5] offset:0
	global_load_dwordx4 v[38:41], v1, s[4:5] offset:1024
	global_load_dwordx4 v[42:45], v1, s[4:5] offset:2048
	global_load_dwordx4 v[46:49], v1, s[4:5] offset:3072
	v_add_u32_e32 v1, 0x3000, v254
	global_load_dwordx4 v[50:53], v1, s[4:5] offset:0
	global_load_dwordx4 v[54:57], v1, s[4:5] offset:1024
	global_load_dwordx4 v[58:61], v1, s[4:5] offset:2048
	global_load_dwordx4 v[62:65], v1, s[4:5] offset:3072
	v_add_u32_e32 v1, 0x4000, v254
	global_load_dwordx4 v[66:69], v1, s[4:5] offset:0
	global_load_dwordx4 v[70:73], v1, s[4:5] offset:1024
	global_load_dwordx4 v[74:77], v1, s[4:5] offset:2048
	global_load_dwordx4 v[78:81], v1, s[4:5] offset:3072
	v_add_u32_e32 v1, 0x5000, v254
	global_load_dwordx4 v[82:85], v1, s[4:5] offset:0
	global_load_dwordx4 v[86:89], v1, s[4:5] offset:1024
	global_load_dwordx4 v[90:93], v1, s[4:5] offset:2048
	global_load_dwordx4 v[94:97], v1, s[4:5] offset:3072
	v_add_u32_e32 v1, 0x8000, v254
	global_load_dwordx4 v[98:101], v1, s[4:5] offset:0
	global_load_dwordx4 v[102:105], v1, s[4:5] offset:1024
	global_load_dwordx4 v[106:109], v1, s[4:5] offset:2048
	global_load_dwordx4 v[110:113], v1, s[4:5] offset:3072
	v_add_u32_e32 v1, 0x9000, v254
	global_load_dwordx4 v[114:117], v1, s[4:5] offset:0
	global_load_dwordx4 v[118:121], v1, s[4:5] offset:1024
	global_load_dwordx4 v[122:125], v1, s[4:5] offset:2048
	global_load_dwordx4 v[126:129], v1, s[4:5] offset:3072
	v_add_u32_e32 v1, 0xa000, v254
	global_load_dwordx4 v[130:133], v1, s[4:5] offset:0
	global_load_dwordx4 v[134:137], v1, s[4:5] offset:1024
	global_load_dwordx4 v[138:141], v1, s[4:5] offset:2048
	global_load_dwordx4 v[142:145], v1, s[4:5] offset:3072
	v_add_u32_e32 v1, 0xb000, v254
	global_load_dwordx4 v[146:149], v1, s[4:5] offset:0
	global_load_dwordx4 v[150:153], v1, s[4:5] offset:1024
	global_load_dwordx4 v[154:157], v1, s[4:5] offset:2048
	global_load_dwordx4 v[158:161], v1, s[4:5] offset:3072
	v_add_u32_e32 v1, 0x6000, v254
	global_load_dwordx4 v[174:177], v1, s[4:5] offset:0
	global_load_dwordx4 v[178:181], v1, s[4:5] offset:1024
	global_load_dwordx4 v[182:185], v1, s[4:5] offset:2048
	global_load_dwordx4 v[186:189], v1, s[4:5] offset:3072
	v_add_u32_e32 v1, 0x7000, v254
	global_load_dwordx4 v[190:193], v1, s[4:5] offset:0
	global_load_dwordx4 v[194:197], v1, s[4:5] offset:1024
	global_load_dwordx4 v[198:201], v1, s[4:5] offset:2048
	global_load_dwordx4 v[202:205], v1, s[4:5] offset:3072
	v_lshlrev_b32_e32 v1, 2, v0
	global_load_dword v206, v1, s[6:7]
	v_add_u32_e32 v245, 0x25000, v1
	s_mul_i32 s22, s2, 48
	v_lshrrev_b32_e32 v1, 5, v0
	v_and_b32_e32 v253, 15, v0
	v_lshlrev_b32_e32 v253, 4, v253
	v_and_b32_e32 v254, 16, v0
	v_mul_u32_u24_e32 v254, 0x271000, v254
	v_add_u32_e32 v253, v253, v254
	v_add_u32_e32 v254, s22, v1
	v_min_u32_e32 v246, 0x270f, v254
	v_lshl_add_u32 v246, v246, 8, v253
	v_add_u32_e32 v254, 16, v254
	v_min_u32_e32 v247, 0x270f, v254
	v_lshl_add_u32 v247, v247, 8, v253
	v_add_u32_e32 v254, 16, v254
	v_min_u32_e32 v248, 0x270f, v254
	v_lshl_add_u32 v248, v248, 8, v253
	v_mul_u32_u24_e32 v249, 0x90, v1
	v_and_b32_e32 v253, 3, v0
	v_mul_u32_u24_e32 v253, 0x1b00, v253
	v_bfe_u32 v254, v0, 2, 3
	v_lshl_add_u32 v253, v254, 4, v253
	v_add_u32_e32 v249, v249, v253
	v_add_u32_e32 v249, 0x10000, v249
	s_add_u32 s12, s8, 0x271000
	s_addc_u32 s13, s9, 0
	global_load_dwordx4 v[234:237], v246, s[8:9]
	global_load_dwordx4 v[238:241], v247, s[8:9]
	global_load_dwordx4 v[210:213], v248, s[8:9]
	global_load_dwordx4 v[214:217], v246, s[12:13]
	s_add_u32 s8, s8, 0x271000
	s_addc_u32 s9, s9, 0
	s_add_u32 s12, s12, 0x271000
	s_addc_u32 s13, s13, 0
	v_lshrrev_b32_e32 v1, 4, v0
	v_mul_u32_u24_e32 v250, 0x50, v1
	v_and_b32_e32 v253, 3, v0
	v_mul_u32_u24_e32 v253, 0xf00, v253
	v_bfe_u32 v254, v0, 2, 2
	v_lshl_add_u32 v253, v254, 4, v253
	v_add_u32_e32 v250, v250, v253
	v_add_u32_e32 v250, 0x1d800, v250
	v_and_b32_e32 v253, 15, v0
	v_add_u32_e32 v254, s22, v1
	v_lshlrev_b32_e32 v251, 8, v254
	v_lshl_add_u32 v251, v253, 4, v251
	s_movk_i32 s23, 0x2710
	v_cmp_gt_u32_e64 s[18:19], s23, v254
	v_add_u32_e32 v254, 32, v254
	v_cmp_gt_u32_e64 s[20:21], s23, v254
	s_movk_i32 s23, 0x100
	v_cmp_gt_u32_e64 s[22:23], s23, v0
	s_nop 3
	s_and_b64 s[20:21], s[20:21], s[22:23]
	s_add_u32 s14, s10, 0x2000
	s_addc_u32 s15, s11, 0
	v_and_b32_e32 v1, 15, v0
	v_bfe_u32 v253, v0, 4, 2
	v_mul_u32_u24_e32 v242, 0x90, v1
	v_mul_u32_u24_e32 v254, 0x1b00, v253
	v_add_u32_e32 v242, v242, v254
	v_add_u32_e32 v242, 0x10000, v242
	v_mul_u32_u24_e32 v243, 0x50, v1
	v_mul_u32_u24_e32 v254, 0xf00, v253
	v_add_u32_e32 v254, v243, v254
	v_add_u32_e32 v254, 0x1d800, v254
	v_lshrrev_b32_e32 v244, 6, v0
	v_lshrrev_b32_e32 v252, 1, v253
	v_and_b32_e32 v1, 1, v244
	v_lshl_add_u32 v252, v1, 1, v252
	v_mul_u32_u24_e32 v252, 0xf00, v252
	v_add_u32_e32 v252, v252, v243
	v_add_u32_e32 v252, 0x1d800, v252
	v_lshrrev_b32_e32 v1, 1, v244
	v_lshl_add_u32 v252, v1, 4, v252
	v_and_b32_e32 v1, 1, v253
	v_lshl_add_u32 v1, v1, 3, v252
	v_mov_b32_e32 v243, v254
	v_lshrrev_b32_e32 v254, 6, v0
	v_mov_b32_e32 v244, v1
	v_mov_b32_e32 v218, 0
	v_mov_b32_e32 v219, 0
	v_mov_b32_e32 v220, 0
	v_mov_b32_e32 v221, 0
	v_mov_b32_e32 v162, 0
	v_mov_b32_e32 v163, 0
	v_mov_b32_e32 v164, 0
	v_mov_b32_e32 v165, 0
	v_mov_b32_e32 v166, 0
	v_mov_b32_e32 v167, 0
	v_mov_b32_e32 v168, 0
	v_mov_b32_e32 v169, 0
	v_mov_b32_e32 v170, 0
	v_mov_b32_e32 v171, 0
	v_mov_b32_e32 v172, 0
	v_mov_b32_e32 v173, 0
	v_mov_b32_e32 v252, 0x4038aa3b
	s_mov_b32 s16, 0xc0b8aa3b
	v_lshlrev_b32_e32 v1, 4, v0
	v_add_u32_e32 v1, 0x1d800, v1
	ds_write_b128 v1, v[218:221]
	ds_write_b128 v1, v[218:221] offset:8192
	s_waitcnt vmcnt(0)
	ds_write_b128 v255, v[174:177] offset:0
	ds_write_b128 v255, v[178:181] offset:1024
	ds_write_b128 v255, v[182:185] offset:2048
	ds_write_b128 v255, v[186:189] offset:3072
	ds_write_b128 v255, v[190:193] offset:4096
	ds_write_b128 v255, v[194:197] offset:5120
	ds_write_b128 v255, v[198:201] offset:6144
	ds_write_b128 v255, v[202:205] offset:7168
	ds_write_b32 v245, v206
	ds_write_b128 v249, v[234:237]
	ds_write_b128 v249, v[238:241] offset:2304
	ds_write_b128 v249, v[210:213] offset:4608
	ds_write_b128 v249, v[214:217] offset:27648
	v_lshlrev_b32_e32 v245, 6, v254
	v_lshl_add_u32 v245, v253, 4, v245
	v_add_u32_e32 v245, 0x25000, v245
	s_waitcnt lgkmcnt(0)
	s_barrier
	ds_read_b128 v[218:221], v255 offset:0
	ds_read_b128 v[222:225], v255 offset:1024
	ds_read_b128 v[226:229], v255 offset:2048
	ds_read_b128 v[230:233], v255 offset:3072
	ds_read_b128 v[174:177], v245 offset:0
	ds_read_b128 v[178:181], v245 offset:512
	ds_read_b128 v[182:185], v245 offset:1024
	ds_read_b128 v[186:189], v245 offset:1536
	ds_read_b128 v[206:209], v242 offset:0
	ds_read_b128 v[210:213], v242 offset:96
	s_waitcnt lgkmcnt(1)
	ds_read_b128 v[214:217], v242 offset:16
	v_mfma_f32_16x16x32_f16 v[174:177], v[2:5], v[206:209], v[174:177]
	v_mfma_f32_16x16x32_f16 v[178:181], v[6:9], v[206:209], v[178:181]
	v_mfma_f32_16x16x32_f16 v[182:185], v[10:13], v[206:209], v[182:185]
	v_mfma_f32_16x16x32_f16 v[186:189], v[14:17], v[206:209], v[186:189]
	s_waitcnt lgkmcnt(1)
	ds_read_b128 v[206:209], v242 offset:32
	v_mfma_f32_16x16x32_f16 v[174:177], v[218:221], v[210:213], v[174:177]
	ds_read_b128 v[218:221], v255 offset:4096
	ds_read_b128 v[190:193], v245 offset:0
	v_mfma_f32_16x16x32_f16 v[178:181], v[222:225], v[210:213], v[178:181]
	ds_read_b128 v[222:225], v255 offset:5120
	ds_read_b128 v[194:197], v245 offset:512
	v_mfma_f32_16x16x32_f16 v[182:185], v[226:229], v[210:213], v[182:185]
	ds_read_b128 v[226:229], v255 offset:6144
	ds_read_b128 v[198:201], v245 offset:1024
	v_mfma_f32_16x16x32_f16 v[186:189], v[230:233], v[210:213], v[186:189]
	ds_read_b128 v[230:233], v255 offset:7168
	ds_read_b128 v[202:205], v245 offset:1536
	s_waitcnt lgkmcnt(9)
	ds_read_b128 v[210:213], v242 offset:112
	v_mfma_f32_16x16x32_f16 v[174:177], v[18:21], v[214:217], v[174:177]
	v_mfma_f32_16x16x32_f16 v[178:181], v[22:25], v[214:217], v[178:181]
	v_mfma_f32_16x16x32_f16 v[182:185], v[26:29], v[214:217], v[182:185]
	v_mfma_f32_16x16x32_f16 v[186:189], v[30:33], v[214:217], v[186:189]
	s_waitcnt lgkmcnt(9)
	ds_read_b128 v[214:217], v242 offset:48
	v_mfma_f32_16x16x32_f16 v[174:177], v[34:37], v[206:209], v[174:177]
	v_mfma_f32_16x16x32_f16 v[178:181], v[38:41], v[206:209], v[178:181]
	v_mfma_f32_16x16x32_f16 v[182:185], v[42:45], v[206:209], v[182:185]
	v_mfma_f32_16x16x32_f16 v[186:189], v[46:49], v[206:209], v[186:189]
	s_waitcnt lgkmcnt(1)
	ds_read_b128 v[206:209], v242 offset:64
	v_mfma_f32_16x16x32_f16 v[174:177], v[218:221], v[210:213], v[174:177]
	ds_read_b128 v[218:221], v255 offset:0
	v_mfma_f32_16x16x32_f16 v[178:181], v[222:225], v[210:213], v[178:181]
	ds_read_b128 v[222:225], v255 offset:1024
	v_mfma_f32_16x16x32_f16 v[182:185], v[226:229], v[210:213], v[182:185]
	ds_read_b128 v[226:229], v255 offset:2048
	v_mfma_f32_16x16x32_f16 v[186:189], v[230:233], v[210:213], v[186:189]
	ds_read_b128 v[230:233], v255 offset:3072
	s_waitcnt lgkmcnt(5)
	ds_read_b128 v[210:213], v242 offset:80
	v_mfma_f32_16x16x32_f16 v[174:177], v[50:53], v[214:217], v[174:177]
	v_mfma_f32_16x16x32_f16 v[178:181], v[54:57], v[214:217], v[178:181]
	v_mfma_f32_16x16x32_f16 v[182:185], v[58:61], v[214:217], v[182:185]
	v_mfma_f32_16x16x32_f16 v[186:189], v[62:65], v[214:217], v[186:189]
	s_waitcnt lgkmcnt(0)
	s_mov_b32 s17, 0
	s_barrier
.Llstm1_loop:
	ds_read_b128 v[234:237], v250 offset:0
	s_mov_b64 exec, s[20:21]
	ds_read_b128 v[238:241], v250 offset:2560
	s_mov_b64 exec, -1
	ds_read_b128 v[214:217], v243 offset:0
	v_mfma_f32_16x16x32_f16 v[174:177], v[66:69], v[206:209], v[174:177]
	v_mfma_f32_16x16x32_f16 v[178:181], v[70:73], v[206:209], v[178:181]
	v_mfma_f32_16x16x32_f16 v[182:185], v[74:77], v[206:209], v[182:185]
	v_mfma_f32_16x16x32_f16 v[186:189], v[78:81], v[206:209], v[186:189]
	ds_read_b128 v[206:209], v243 offset:16
	v_mfma_f32_16x16x32_f16 v[174:177], v[82:85], v[210:213], v[174:177]
	v_mfma_f32_16x16x32_f16 v[178:181], v[86:89], v[210:213], v[178:181]
	v_mfma_f32_16x16x32_f16 v[182:185], v[90:93], v[210:213], v[182:185]
	v_mfma_f32_16x16x32_f16 v[186:189], v[94:97], v[210:213], v[186:189]
	s_waitcnt lgkmcnt(2)
	s_cmp_eq_u32 s17, 0
	s_cbranch_scc1 .Lskipy77
	s_mov_b64 exec, s[18:19]
	global_store_dwordx4 v251, v[234:237], s[10:11]
	s_mov_b64 exec, s[20:21]
	global_store_dwordx4 v251, v[238:241], s[14:15]
	s_mov_b64 exec, -1
	s_add_u32 s10, s10, 0x271000
	s_addc_u32 s11, s11, 0
	s_add_u32 s14, s14, 0x271000
	s_addc_u32 s15, s15, 0
.Lskipy77:
	s_waitcnt lgkmcnt(1)
	ds_read_b128 v[210:213], v243 offset:32
	v_mfma_f32_16x16x32_f16 v[174:177], v[98:101], v[214:217], v[174:177]
	v_mfma_f32_16x16x32_f16 v[178:181], v[102:105], v[214:217], v[178:181]
	v_mfma_f32_16x16x32_f16 v[182:185], v[106:109], v[214:217], v[182:185]
	v_mfma_f32_16x16x32_f16 v[186:189], v[110:113], v[214:217], v[186:189]
	global_load_dwordx4 v[234:237], v246, s[12:13]
	s_waitcnt lgkmcnt(1)
	ds_read_b128 v[214:217], v243 offset:48
	v_mfma_f32_16x16x32_f16 v[174:177], v[114:117], v[206:209], v[174:177]
	v_mfma_f32_16x16x32_f16 v[178:181], v[118:121], v[206:209], v[178:181]
	v_mfma_f32_16x16x32_f16 v[182:185], v[122:125], v[206:209], v[182:185]
	v_mfma_f32_16x16x32_f16 v[186:189], v[126:129], v[206:209], v[186:189]
	global_load_dwordx4 v[238:241], v247, s[8:9]
	s_waitcnt lgkmcnt(1)
	ds_read_b128 v[206:209], v242 offset:2304
	v_mfma_f32_16x16x32_f16 v[174:177], v[130:133], v[210:213], v[174:177]
	v_mfma_f32_16x16x32_f16 v[178:181], v[134:137], v[210:213], v[178:181]
	v_mfma_f32_16x16x32_f16 v[182:185], v[138:141], v[210:213], v[182:185]
	v_mfma_f32_16x16x32_f16 v[186:189], v[142:145], v[210:213], v[186:189]
	s_add_u32 s12, s12, 0x271000
	s_waitcnt lgkmcnt(1)
	ds_read_b128 v[210:213], v242 offset:2320
	v_mfma_f32_16x16x32_f16 v[174:177], v[146:149], v[214:217], v[174:177]
	v_mfma_f32_16x16x32_f16 v[178:181], v[150:153], v[214:217], v[178:181]
	v_mfma_f32_16x16x32_f16 v[182:185], v[154:157], v[214:217], v[182:185]
	v_mfma_f32_16x16x32_f16 v[186:189], v[158:161], v[214:217], v[186:189]
	s_addc_u32 s13, s13, 0
	s_waitcnt lgkmcnt(1)
	ds_read_b128 v[214:217], v242 offset:2400
	v_mfma_f32_16x16x32_f16 v[190:193], v[2:5], v[206:209], v[190:193]
	v_mfma_f32_16x16x32_f16 v[194:197], v[6:9], v[206:209], v[194:197]
	v_mfma_f32_16x16x32_f16 v[198:201], v[10:13], v[206:209], v[198:201]
	v_mfma_f32_16x16x32_f16 v[202:205], v[14:17], v[206:209], v[202:205]
	s_waitcnt lgkmcnt(1)
	ds_read_b128 v[206:209], v242 offset:2336
	v_mfma_f32_16x16x32_f16 v[190:193], v[18:21], v[210:213], v[190:193]
	v_mfma_f32_16x16x32_f16 v[194:197], v[22:25], v[210:213], v[194:197]
	v_mfma_f32_16x16x32_f16 v[198:201], v[26:29], v[210:213], v[198:201]
	v_mfma_f32_16x16x32_f16 v[202:205], v[30:33], v[210:213], v[202:205]
	s_waitcnt lgkmcnt(1)
	ds_read_b128 v[210:213], v242 offset:2352
	v_mfma_f32_16x16x32_f16 v[190:193], v[218:221], v[214:217], v[190:193]
	ds_read_b128 v[218:221], v255 offset:4096
	v_exp_f32_e32 v174, v174
	v_exp_f32_e32 v175, v175
	v_mfma_f32_16x16x32_f16 v[194:197], v[222:225], v[214:217], v[194:197]
	ds_read_b128 v[222:225], v255 offset:5120
	v_exp_f32_e32 v178, v178
	v_exp_f32_e32 v179, v179
	v_mfma_f32_16x16x32_f16 v[198:201], v[226:229], v[214:217], v[198:201]
	ds_read_b128 v[226:229], v255 offset:6144
	v_exp_f32_e32 v182, v182
	v_exp_f32_e32 v183, v183
	v_mfma_f32_16x16x32_f16 v[202:205], v[230:233], v[214:217], v[202:205]
	ds_read_b128 v[230:233], v255 offset:7168
	v_exp_f32_e32 v186, v186
	v_exp_f32_e32 v187, v187
	s_waitcnt lgkmcnt(5)
	ds_read_b128 v[214:217], v243 offset:1280
	v_mfma_f32_16x16x32_f16 v[190:193], v[34:37], v[206:209], v[190:193]
	v_add_f32_e32 v182, 1.0, v182
	v_add_f32_e32 v183, 1.0, v183
	v_mfma_f32_16x16x32_f16 v[194:197], v[38:41], v[206:209], v[194:197]
	v_add_f32_e32 v178, 1.0, v178
	v_add_f32_e32 v179, 1.0, v179
	v_mfma_f32_16x16x32_f16 v[198:201], v[42:45], v[206:209], v[198:201]
	v_fma_f32 v174, v174, v182, v182
	v_fma_f32 v175, v175, v183, v183
	v_mfma_f32_16x16x32_f16 v[202:205], v[46:49], v[206:209], v[202:205]
	v_rcp_f32_e32 v178, v178
	v_rcp_f32_e32 v179, v179
	v_fma_f32 v182, v182, v252, s16
	s_waitcnt lgkmcnt(5)
	ds_read_b128 v[206:209], v243 offset:1296
	v_mfma_f32_16x16x32_f16 v[190:193], v[50:53], v[210:213], v[190:193]
	v_fma_f32 v183, v183, v252, s16
	v_rcp_f32_e32 v174, v174
	v_mfma_f32_16x16x32_f16 v[194:197], v[54:57], v[210:213], v[194:197]
	v_rcp_f32_e32 v175, v175
	v_mul_f32_e32 v162, v162, v178
	v_mfma_f32_16x16x32_f16 v[198:201], v[58:61], v[210:213], v[198:201]
	v_mul_f32_e32 v163, v163, v179
	v_fma_f32 v162, v182, v174, v162
	v_mfma_f32_16x16x32_f16 v[202:205], v[62:65], v[210:213], v[202:205]
	v_fma_f32 v163, v183, v175, v163
	v_exp_f32_e32 v178, v162
	v_exp_f32_e32 v179, v163
	s_waitcnt lgkmcnt(1)
	ds_read_b128 v[210:213], v242 offset:2416
	v_mfma_f32_16x16x32_f16 v[190:193], v[98:101], v[214:217], v[190:193]
	v_add_f32_e32 v174, 1.0, v178
	v_add_f32_e32 v175, 1.0, v179
	v_mfma_f32_16x16x32_f16 v[194:197], v[102:105], v[214:217], v[194:197]
	v_add_f32_e32 v182, -1.0, v178
	v_add_f32_e32 v183, -1.0, v179
	v_mfma_f32_16x16x32_f16 v[198:201], v[106:109], v[214:217], v[198:201]
	v_fma_f32 v186, v186, v174, v174
	v_fma_f32 v187, v187, v175, v175
	v_mfma_f32_16x16x32_f16 v[202:205], v[110:113], v[214:217], v[202:205]
	v_rcp_f32_e32 v186, v186
	v_rcp_f32_e32 v187, v187
	v_mul_f32_e32 v186, v182, v186
	s_waitcnt lgkmcnt(1)
	ds_read_b128 v[214:217], v242 offset:2368
	v_mfma_f32_16x16x32_f16 v[190:193], v[114:117], v[206:209], v[190:193]
	v_mul_f32_e32 v187, v183, v187
	v_exp_f32_e32 v176, v176
	v_mfma_f32_16x16x32_f16 v[194:197], v[118:121], v[206:209], v[194:197]
	v_exp_f32_e32 v177, v177
	v_exp_f32_e32 v180, v180
	v_mfma_f32_16x16x32_f16 v[198:201], v[122:125], v[206:209], v[198:201]
	v_exp_f32_e32 v181, v181
	v_exp_f32_e32 v184, v184
	v_mfma_f32_16x16x32_f16 v[202:205], v[126:129], v[206:209], v[202:205]
	v_exp_f32_e32 v185, v185
	v_exp_f32_e32 v188, v188
	s_waitcnt lgkmcnt(1)
	ds_read_b128 v[206:209], v242 offset:2384
	v_mfma_f32_16x16x32_f16 v[190:193], v[218:221], v[210:213], v[190:193]
	ds_read_b128 v[218:221], v255 offset:0
	v_exp_f32_e32 v189, v189
	v_add_f32_e32 v184, 1.0, v184
	v_mfma_f32_16x16x32_f16 v[194:197], v[222:225], v[210:213], v[194:197]
	ds_read_b128 v[222:225], v255 offset:1024
	v_add_f32_e32 v185, 1.0, v185
	v_add_f32_e32 v180, 1.0, v180
	v_mfma_f32_16x16x32_f16 v[198:201], v[226:229], v[210:213], v[198:201]
	ds_read_b128 v[226:229], v255 offset:2048
	v_add_f32_e32 v181, 1.0, v181
	v_fma_f32 v176, v176, v184, v184
	v_mfma_f32_16x16x32_f16 v[202:205], v[230:233], v[210:213], v[202:205]
	ds_read_b128 v[230:233], v255 offset:3072
	v_fma_f32 v177, v177, v185, v185
	v_rcp_f32_e32 v180, v180
	v_rcp_f32_e32 v181, v181
	s_waitcnt lgkmcnt(5)
	ds_read_b128 v[210:213], v243 offset:1312
	v_mfma_f32_16x16x32_f16 v[190:193], v[66:69], v[214:217], v[190:193]
	v_fma_f32 v184, v184, v252, s16
	v_fma_f32 v185, v185, v252, s16
	v_mfma_f32_16x16x32_f16 v[194:197], v[70:73], v[214:217], v[194:197]
	v_rcp_f32_e32 v176, v176
	v_rcp_f32_e32 v177, v177
	v_mfma_f32_16x16x32_f16 v[198:201], v[74:77], v[214:217], v[198:201]
	v_mul_f32_e32 v164, v164, v180
	v_mul_f32_e32 v165, v165, v181
	v_mfma_f32_16x16x32_f16 v[202:205], v[78:81], v[214:217], v[202:205]
	v_fma_f32 v164, v184, v176, v164
	v_fma_f32 v165, v185, v177, v165
	v_exp_f32_e32 v180, v164
	s_waitcnt lgkmcnt(5)
	ds_read_b128 v[214:217], v243 offset:1328
	v_mfma_f32_16x16x32_f16 v[190:193], v[82:85], v[206:209], v[190:193]
	s_waitcnt vmcnt(0)
	ds_write_b128 v249, v[234:237] offset:0
	ds_write_b128 v249, v[238:241] offset:29952
	global_load_dwordx4 v[234:237], v248, s[8:9]
	s_add_u32 s8, s8, 0x271000
	s_addc_u32 s9, s9, 0
	v_exp_f32_e32 v181, v165
	v_mfma_f32_16x16x32_f16 v[194:197], v[86:89], v[206:209], v[194:197]
	v_add_f32_e32 v176, 1.0, v180
	v_add_f32_e32 v177, 1.0, v181
	v_add_f32_e32 v184, -1.0, v180
	v_mfma_f32_16x16x32_f16 v[198:201], v[90:93], v[206:209], v[198:201]
	v_add_f32_e32 v185, -1.0, v181
	v_fma_f32 v188, v188, v176, v176
	v_mfma_f32_16x16x32_f16 v[202:205], v[94:97], v[206:209], v[202:205]
	v_fma_f32 v189, v189, v177, v177
	v_rcp_f32_e32 v188, v188
	v_rcp_f32_e32 v189, v189
	s_waitcnt lgkmcnt(3)
	ds_read_b128 v[206:209], v242 offset:4608
	v_mfma_f32_16x16x32_f16 v[190:193], v[130:133], v[210:213], v[190:193]
	v_mul_f32_e32 v188, v184, v188
	v_mul_f32_e32 v189, v185, v189
	v_mfma_f32_16x16x32_f16 v[194:197], v[134:137], v[210:213], v[194:197]
	v_cvt_pk_f16_f32 v186, v186, v187
	v_cvt_pk_f16_f32 v187, v188, v189
	v_mfma_f32_16x16x32_f16 v[198:201], v[138:141], v[210:213], v[198:201]
	ds_write_b64 v244, v[186:187] offset:15360
	ds_read_b128 v[174:177], v245 offset:0
	v_mfma_f32_16x16x32_f16 v[202:205], v[142:145], v[210:213], v[202:205]
	ds_read_b128 v[178:181], v245 offset:512
	ds_read_b128 v[182:185], v245 offset:1024
	ds_read_b128 v[186:189], v245 offset:1536
	s_waitcnt lgkmcnt(8)
	ds_read_b128 v[210:213], v242 offset:4624
	v_mfma_f32_16x16x32_f16 v[190:193], v[146:149], v[214:217], v[190:193]
	v_mfma_f32_16x16x32_f16 v[194:197], v[150:153], v[214:217], v[194:197]
	v_mfma_f32_16x16x32_f16 v[198:201], v[154:157], v[214:217], v[198:201]
	v_mfma_f32_16x16x32_f16 v[202:205], v[158:161], v[214:217], v[202:205]
	s_waitcnt lgkmcnt(6)
	ds_read_b128 v[214:217], v242 offset:4704
	s_waitcnt lgkmcnt(5)
	v_mfma_f32_16x16x32_f16 v[174:177], v[2:5], v[206:209], v[174:177]
	s_waitcnt lgkmcnt(4)
	v_mfma_f32_16x16x32_f16 v[178:181], v[6:9], v[206:209], v[178:181]
	s_waitcnt lgkmcnt(3)
	v_mfma_f32_16x16x32_f16 v[182:185], v[10:13], v[206:209], v[182:185]
	s_waitcnt lgkmcnt(2)
	v_mfma_f32_16x16x32_f16 v[186:189], v[14:17], v[206:209], v[186:189]
	s_waitcnt lgkmcnt(1)
	ds_read_b128 v[206:209], v242 offset:4640
	v_mfma_f32_16x16x32_f16 v[174:177], v[18:21], v[210:213], v[174:177]
	v_mfma_f32_16x16x32_f16 v[178:181], v[22:25], v[210:213], v[178:181]
	v_mfma_f32_16x16x32_f16 v[182:185], v[26:29], v[210:213], v[182:185]
	v_mfma_f32_16x16x32_f16 v[186:189], v[30:33], v[210:213], v[186:189]
	s_waitcnt lgkmcnt(1)
	ds_read_b128 v[210:213], v242 offset:4656
	v_mfma_f32_16x16x32_f16 v[174:177], v[218:221], v[214:217], v[174:177]
	ds_read_b128 v[218:221], v255 offset:4096
	v_exp_f32_e32 v190, v190
	v_exp_f32_e32 v191, v191
	v_mfma_f32_16x16x32_f16 v[178:181], v[222:225], v[214:217], v[178:181]
	ds_read_b128 v[222:225], v255 offset:5120
	v_exp_f32_e32 v194, v194
	v_exp_f32_e32 v195, v195
	v_mfma_f32_16x16x32_f16 v[182:185], v[226:229], v[214:217], v[182:185]
	ds_read_b128 v[226:229], v255 offset:6144
	v_exp_f32_e32 v198, v198
	v_exp_f32_e32 v199, v199
	v_mfma_f32_16x16x32_f16 v[186:189], v[230:233], v[214:217], v[186:189]
	ds_read_b128 v[230:233], v255 offset:7168
	v_exp_f32_e32 v202, v202
	v_exp_f32_e32 v203, v203
	s_waitcnt lgkmcnt(5)
	ds_read_b128 v[214:217], v243 offset:2560
	v_mfma_f32_16x16x32_f16 v[174:177], v[34:37], v[206:209], v[174:177]
	v_add_f32_e32 v198, 1.0, v198
	v_add_f32_e32 v199, 1.0, v199
	v_mfma_f32_16x16x32_f16 v[178:181], v[38:41], v[206:209], v[178:181]
	v_add_f32_e32 v194, 1.0, v194
	v_add_f32_e32 v195, 1.0, v195
	v_mfma_f32_16x16x32_f16 v[182:185], v[42:45], v[206:209], v[182:185]
	v_fma_f32 v190, v190, v198, v198
	v_fma_f32 v191, v191, v199, v199
	v_mfma_f32_16x16x32_f16 v[186:189], v[46:49], v[206:209], v[186:189]
	v_rcp_f32_e32 v194, v194
	v_rcp_f32_e32 v195, v195
	v_fma_f32 v198, v198, v252, s16
	s_waitcnt lgkmcnt(5)
	ds_read_b128 v[206:209], v243 offset:2576
	v_mfma_f32_16x16x32_f16 v[174:177], v[50:53], v[210:213], v[174:177]
	v_fma_f32 v199, v199, v252, s16
	v_rcp_f32_e32 v190, v190
	v_mfma_f32_16x16x32_f16 v[178:181], v[54:57], v[210:213], v[178:181]
	v_rcp_f32_e32 v191, v191
	v_mul_f32_e32 v166, v166, v194
	v_mfma_f32_16x16x32_f16 v[182:185], v[58:61], v[210:213], v[182:185]
	v_mul_f32_e32 v167, v167, v195
	v_fma_f32 v166, v198, v190, v166
	v_mfma_f32_16x16x32_f16 v[186:189], v[62:65], v[210:213], v[186:189]
	v_fma_f32 v167, v199, v191, v167
	v_exp_f32_e32 v194, v166
	v_exp_f32_e32 v195, v167
	s_waitcnt lgkmcnt(1)
	ds_read_b128 v[210:213], v242 offset:4720
	v_mfma_f32_16x16x32_f16 v[174:177], v[98:101], v[214:217], v[174:177]
	v_add_f32_e32 v190, 1.0, v194
	v_add_f32_e32 v191, 1.0, v195
	v_mfma_f32_16x16x32_f16 v[178:181], v[102:105], v[214:217], v[178:181]
	v_add_f32_e32 v198, -1.0, v194
	v_add_f32_e32 v199, -1.0, v195
	v_mfma_f32_16x16x32_f16 v[182:185], v[106:109], v[214:217], v[182:185]
	v_fma_f32 v202, v202, v190, v190
	v_fma_f32 v203, v203, v191, v191
	v_mfma_f32_16x16x32_f16 v[186:189], v[110:113], v[214:217], v[186:189]
	v_rcp_f32_e32 v202, v202
	v_rcp_f32_e32 v203, v203
	v_mul_f32_e32 v202, v198, v202
	s_waitcnt lgkmcnt(1)
	ds_read_b128 v[214:217], v242 offset:4672
	v_mfma_f32_16x16x32_f16 v[174:177], v[114:117], v[206:209], v[174:177]
	v_mul_f32_e32 v203, v199, v203
	v_exp_f32_e32 v192, v192
	v_mfma_f32_16x16x32_f16 v[178:181], v[118:121], v[206:209], v[178:181]
	v_exp_f32_e32 v193, v193
	v_exp_f32_e32 v196, v196
	v_mfma_f32_16x16x32_f16 v[182:185], v[122:125], v[206:209], v[182:185]
	v_exp_f32_e32 v197, v197
	v_exp_f32_e32 v200, v200
	v_mfma_f32_16x16x32_f16 v[186:189], v[126:129], v[206:209], v[186:189]
	v_exp_f32_e32 v201, v201
	v_exp_f32_e32 v204, v204
	s_waitcnt lgkmcnt(1)
	ds_read_b128 v[206:209], v242 offset:4688
	v_mfma_f32_16x16x32_f16 v[174:177], v[218:221], v[210:213], v[174:177]
	ds_read_b128 v[218:221], v255 offset:0
	v_exp_f32_e32 v205, v205
	v_add_f32_e32 v200, 1.0, v200
	v_mfma_f32_16x16x32_f16 v[178:181], v[222:225], v[210:213], v[178:181]
	ds_read_b128 v[222:225], v255 offset:1024
	v_add_f32_e32 v201, 1.0, v201
	v_add_f32_e32 v196, 1.0, v196
	v_mfma_f32_16x16x32_f16 v[182:185], v[226:229], v[210:213], v[182:185]
	ds_read_b128 v[226:229], v255 offset:2048
	v_add_f32_e32 v197, 1.0, v197
	v_fma_f32 v192, v192, v200, v200
	v_mfma_f32_16x16x32_f16 v[186:189], v[230:233], v[210:213], v[186:189]
	ds_read_b128 v[230:233], v255 offset:3072
	v_fma_f32 v193, v193, v201, v201
	v_rcp_f32_e32 v196, v196
	v_rcp_f32_e32 v197, v197
	s_waitcnt lgkmcnt(5)
	ds_read_b128 v[210:213], v243 offset:2592
	v_mfma_f32_16x16x32_f16 v[174:177], v[66:69], v[214:217], v[174:177]
	v_fma_f32 v200, v200, v252, s16
	v_fma_f32 v201, v201, v252, s16
	v_mfma_f32_16x16x32_f16 v[178:181], v[70:73], v[214:217], v[178:181]
	v_rcp_f32_e32 v192, v192
	v_rcp_f32_e32 v193, v193
	v_mfma_f32_16x16x32_f16 v[182:185], v[74:77], v[214:217], v[182:185]
	v_mul_f32_e32 v168, v168, v196
	v_mul_f32_e32 v169, v169, v197
	v_mfma_f32_16x16x32_f16 v[186:189], v[78:81], v[214:217], v[186:189]
	v_fma_f32 v168, v200, v192, v168
	v_fma_f32 v169, v201, v193, v169
	v_exp_f32_e32 v196, v168
	s_waitcnt lgkmcnt(5)
	ds_read_b128 v[214:217], v243 offset:2608
	v_mfma_f32_16x16x32_f16 v[174:177], v[82:85], v[206:209], v[174:177]
	v_exp_f32_e32 v197, v169
	v_add_f32_e32 v192, 1.0, v196
	v_mfma_f32_16x16x32_f16 v[178:181], v[86:89], v[206:209], v[178:181]
	v_add_f32_e32 v193, 1.0, v197
	v_add_f32_e32 v200, -1.0, v196
	v_mfma_f32_16x16x32_f16 v[182:185], v[90:93], v[206:209], v[182:185]
	v_add_f32_e32 v201, -1.0, v197
	v_fma_f32 v204, v204, v192, v192
	v_mfma_f32_16x16x32_f16 v[186:189], v[94:97], v[206:209], v[186:189]
	v_fma_f32 v205, v205, v193, v193
	v_rcp_f32_e32 v204, v204
	v_rcp_f32_e32 v205, v205
	s_waitcnt lgkmcnt(1)
	ds_read_b128 v[206:209], v242 offset:27648
	v_mfma_f32_16x16x32_f16 v[174:177], v[130:133], v[210:213], v[174:177]
	v_mul_f32_e32 v204, v200, v204
	v_mul_f32_e32 v205, v201, v205
	v_mfma_f32_16x16x32_f16 v[178:181], v[134:137], v[210:213], v[178:181]
	v_cvt_pk_f16_f32 v202, v202, v203
	v_cvt_pk_f16_f32 v203, v204, v205
	v_mfma_f32_16x16x32_f16 v[182:185], v[138:141], v[210:213], v[182:185]
	ds_write_b64 v244, v[202:203] offset:16640
	ds_read_b128 v[190:193], v245 offset:0
	v_mfma_f32_16x16x32_f16 v[186:189], v[142:145], v[210:213], v[186:189]
	ds_read_b128 v[194:197], v245 offset:512
	ds_read_b128 v[198:201], v245 offset:1024
	ds_read_b128 v[202:205], v245 offset:1536
	s_waitcnt lgkmcnt(6)
	ds_read_b128 v[210:213], v242 offset:27744
	v_mfma_f32_16x16x32_f16 v[174:177], v[146:149], v[214:217], v[174:177]
	v_mfma_f32_16x16x32_f16 v[178:181], v[150:153], v[214:217], v[178:181]
	v_mfma_f32_16x16x32_f16 v[182:185], v[154:157], v[214:217], v[182:185]
	v_mfma_f32_16x16x32_f16 v[186:189], v[158:161], v[214:217], v[186:189]
	s_waitcnt vmcnt(0)
	ds_write_b128 v249, v[234:237] offset:32256
	s_waitcnt lgkmcnt(7)
	ds_read_b128 v[214:217], v242 offset:27664
	s_waitcnt lgkmcnt(6)
	v_mfma_f32_16x16x32_f16 v[190:193], v[2:5], v[206:209], v[190:193]
	s_waitcnt lgkmcnt(5)
	v_mfma_f32_16x16x32_f16 v[194:197], v[6:9], v[206:209], v[194:197]
	s_waitcnt lgkmcnt(4)
	v_mfma_f32_16x16x32_f16 v[198:201], v[10:13], v[206:209], v[198:201]
	s_waitcnt lgkmcnt(3)
	v_mfma_f32_16x16x32_f16 v[202:205], v[14:17], v[206:209], v[202:205]
	s_waitcnt lgkmcnt(2)
	ds_read_b128 v[206:209], v242 offset:27680
	v_mfma_f32_16x16x32_f16 v[190:193], v[218:221], v[210:213], v[190:193]
	ds_read_b128 v[218:221], v255 offset:4096
	v_exp_f32_e32 v174, v174
	v_exp_f32_e32 v175, v175
	v_exp_f32_e32 v178, v178
	v_mfma_f32_16x16x32_f16 v[194:197], v[222:225], v[210:213], v[194:197]
	ds_read_b128 v[222:225], v255 offset:5120
	v_exp_f32_e32 v179, v179
	v_exp_f32_e32 v182, v182
	v_exp_f32_e32 v183, v183
	v_exp_f32_e32 v186, v186
	v_mfma_f32_16x16x32_f16 v[198:201], v[226:229], v[210:213], v[198:201]
	ds_read_b128 v[226:229], v255 offset:6144
	v_exp_f32_e32 v187, v187
	v_add_f32_e32 v182, 1.0, v182
	v_add_f32_e32 v183, 1.0, v183
	v_add_f32_e32 v178, 1.0, v178
	v_mfma_f32_16x16x32_f16 v[202:205], v[230:233], v[210:213], v[202:205]
	ds_read_b128 v[230:233], v255 offset:7168
	v_add_f32_e32 v179, 1.0, v179
	v_fma_f32 v174, v174, v182, v182
	v_fma_f32 v175, v175, v183, v183
	v_rcp_f32_e32 v178, v178
	s_waitcnt lgkmcnt(5)
	ds_read_b128 v[210:213], v242 offset:27760
	v_mfma_f32_16x16x32_f16 v[190:193], v[18:21], v[214:217], v[190:193]
	v_rcp_f32_e32 v179, v179
	v_fma_f32 v182, v182, v252, s16
	v_fma_f32 v183, v183, v252, s16
	v_rcp_f32_e32 v174, v174
	v_mfma_f32_16x16x32_f16 v[194:197], v[22:25], v[214:217], v[194:197]
	v_rcp_f32_e32 v175, v175
	v_mul_f32_e32 v170, v170, v178
	v_mul_f32_e32 v171, v171, v179
	v_fma_f32 v170, v182, v174, v170
	v_mfma_f32_16x16x32_f16 v[198:201], v[26:29], v[214:217], v[198:201]
	v_fma_f32 v171, v183, v175, v171
	v_exp_f32_e32 v178, v170
	v_exp_f32_e32 v179, v171
	v_add_f32_e32 v174, 1.0, v178
	v_mfma_f32_16x16x32_f16 v[202:205], v[30:33], v[214:217], v[202:205]
	v_add_f32_e32 v175, 1.0, v179
	v_add_f32_e32 v182, -1.0, v178
	v_add_f32_e32 v183, -1.0, v179
	v_fma_f32 v186, v186, v174, v174
	s_waitcnt lgkmcnt(5)
	ds_read_b128 v[214:217], v242 offset:27696
	v_mfma_f32_16x16x32_f16 v[190:193], v[34:37], v[206:209], v[190:193]
	v_fma_f32 v187, v187, v175, v175
	v_rcp_f32_e32 v186, v186
	v_rcp_f32_e32 v187, v187
	v_mul_f32_e32 v186, v182, v186
	v_mfma_f32_16x16x32_f16 v[194:197], v[38:41], v[206:209], v[194:197]
	v_mul_f32_e32 v187, v183, v187
	v_exp_f32_e32 v176, v176
	v_exp_f32_e32 v177, v177
	v_exp_f32_e32 v180, v180
	v_mfma_f32_16x16x32_f16 v[198:201], v[42:45], v[206:209], v[198:201]
	v_exp_f32_e32 v181, v181
	v_exp_f32_e32 v184, v184
	v_exp_f32_e32 v185, v185
	v_exp_f32_e32 v188, v188
	v_mfma_f32_16x16x32_f16 v[202:205], v[46:49], v[206:209], v[202:205]
	v_exp_f32_e32 v189, v189
	v_add_f32_e32 v184, 1.0, v184
	v_add_f32_e32 v185, 1.0, v185
	v_add_f32_e32 v180, 1.0, v180
	s_waitcnt lgkmcnt(1)
	ds_read_b128 v[206:209], v242 offset:27712
	v_mfma_f32_16x16x32_f16 v[190:193], v[218:221], v[210:213], v[190:193]
	ds_read_b128 v[218:221], v255 offset:0
	v_add_f32_e32 v181, 1.0, v181
	v_fma_f32 v176, v176, v184, v184
	v_fma_f32 v177, v177, v185, v185
	v_rcp_f32_e32 v180, v180
	v_mfma_f32_16x16x32_f16 v[194:197], v[222:225], v[210:213], v[194:197]
	ds_read_b128 v[222:225], v255 offset:1024
	v_rcp_f32_e32 v181, v181
	v_fma_f32 v184, v184, v252, s16
	v_fma_f32 v185, v185, v252, s16
	v_rcp_f32_e32 v176, v176
	v_mfma_f32_16x16x32_f16 v[198:201], v[226:229], v[210:213], v[198:201]
	ds_read_b128 v[226:229], v255 offset:2048
	v_rcp_f32_e32 v177, v177
	v_mul_f32_e32 v172, v172, v180
	v_mul_f32_e32 v173, v173, v181
	v_fma_f32 v172, v184, v176, v172
	v_mfma_f32_16x16x32_f16 v[202:205], v[230:233], v[210:213], v[202:205]
	ds_read_b128 v[230:233], v255 offset:3072
	v_fma_f32 v173, v185, v177, v173
	v_exp_f32_e32 v180, v172
	v_exp_f32_e32 v181, v173
	v_add_f32_e32 v176, 1.0, v180
	s_waitcnt lgkmcnt(5)
	ds_read_b128 v[210:213], v242 offset:27728
	v_mfma_f32_16x16x32_f16 v[190:193], v[50:53], v[214:217], v[190:193]
	v_add_f32_e32 v177, 1.0, v181
	v_add_f32_e32 v184, -1.0, v180
	v_add_f32_e32 v185, -1.0, v181
	v_fma_f32 v188, v188, v176, v176
	v_mfma_f32_16x16x32_f16 v[194:197], v[54:57], v[214:217], v[194:197]
	v_fma_f32 v189, v189, v177, v177
	v_rcp_f32_e32 v188, v188
	v_rcp_f32_e32 v189, v189
	v_mul_f32_e32 v188, v184, v188
	v_mfma_f32_16x16x32_f16 v[198:201], v[58:61], v[214:217], v[198:201]
	v_mul_f32_e32 v189, v185, v189
	v_cvt_pk_f16_f32 v186, v186, v187
	v_cvt_pk_f16_f32 v187, v188, v189
	ds_write_b64 v244, v[186:187] offset:17920
	v_mfma_f32_16x16x32_f16 v[202:205], v[62:65], v[214:217], v[202:205]
	ds_read_b128 v[174:177], v245 offset:0
	ds_read_b128 v[178:181], v245 offset:512
	ds_read_b128 v[182:185], v245 offset:1024
	ds_read_b128 v[186:189], v245 offset:1536
	s_waitcnt lgkmcnt(0)
	s_barrier
	ds_read_b128 v[234:237], v250 offset:15360
	s_mov_b64 exec, s[20:21]
	ds_read_b128 v[238:241], v250 offset:17920
	s_mov_b64 exec, -1
	ds_read_b128 v[214:217], v243 offset:15360
	v_mfma_f32_16x16x32_f16 v[190:193], v[66:69], v[206:209], v[190:193]
	v_mfma_f32_16x16x32_f16 v[194:197], v[70:73], v[206:209], v[194:197]
	v_mfma_f32_16x16x32_f16 v[198:201], v[74:77], v[206:209], v[198:201]
	v_mfma_f32_16x16x32_f16 v[202:205], v[78:81], v[206:209], v[202:205]
	ds_read_b128 v[206:209], v243 offset:15376
	v_mfma_f32_16x16x32_f16 v[190:193], v[82:85], v[210:213], v[190:193]
	v_mfma_f32_16x16x32_f16 v[194:197], v[86:89], v[210:213], v[194:197]
	v_mfma_f32_16x16x32_f16 v[198:201], v[90:93], v[210:213], v[198:201]
	v_mfma_f32_16x16x32_f16 v[202:205], v[94:97], v[210:213], v[202:205]
	s_waitcnt lgkmcnt(2)
	s_mov_b64 exec, s[18:19]
	global_store_dwordx4 v251, v[234:237], s[10:11]
	s_mov_b64 exec, s[20:21]
	global_store_dwordx4 v251, v[238:241], s[14:15]
	s_mov_b64 exec, -1
	s_add_u32 s10, s10, 0x271000
	s_addc_u32 s11, s11, 0
	s_add_u32 s14, s14, 0x271000
	s_addc_u32 s15, s15, 0
	s_waitcnt lgkmcnt(1)
	ds_read_b128 v[210:213], v243 offset:15392
	v_mfma_f32_16x16x32_f16 v[190:193], v[98:101], v[214:217], v[190:193]
	v_mfma_f32_16x16x32_f16 v[194:197], v[102:105], v[214:217], v[194:197]
	v_mfma_f32_16x16x32_f16 v[198:201], v[106:109], v[214:217], v[198:201]
	v_mfma_f32_16x16x32_f16 v[202:205], v[110:113], v[214:217], v[202:205]
	global_load_dwordx4 v[234:237], v246, s[12:13]
	s_waitcnt lgkmcnt(1)
	ds_read_b128 v[214:217], v243 offset:15408
	v_mfma_f32_16x16x32_f16 v[190:193], v[114:117], v[206:209], v[190:193]
	v_mfma_f32_16x16x32_f16 v[194:197], v[118:121], v[206:209], v[194:197]
	v_mfma_f32_16x16x32_f16 v[198:201], v[122:125], v[206:209], v[198:201]
	v_mfma_f32_16x16x32_f16 v[202:205], v[126:129], v[206:209], v[202:205]
	global_load_dwordx4 v[238:241], v247, s[8:9]
	s_waitcnt lgkmcnt(1)
	ds_read_b128 v[206:209], v242 offset:29952
	v_mfma_f32_16x16x32_f16 v[190:193], v[130:133], v[210:213], v[190:193]
	v_mfma_f32_16x16x32_f16 v[194:197], v[134:137], v[210:213], v[194:197]
	v_mfma_f32_16x16x32_f16 v[198:201], v[138:141], v[210:213], v[198:201]
	v_mfma_f32_16x16x32_f16 v[202:205], v[142:145], v[210:213], v[202:205]
	s_add_u32 s12, s12, 0x271000
	s_waitcnt lgkmcnt(1)
	ds_read_b128 v[210:213], v242 offset:29968
	v_mfma_f32_16x16x32_f16 v[190:193], v[146:149], v[214:217], v[190:193]
	v_mfma_f32_16x16x32_f16 v[194:197], v[150:153], v[214:217], v[194:197]
	v_mfma_f32_16x16x32_f16 v[198:201], v[154:157], v[214:217], v[198:201]
	v_mfma_f32_16x16x32_f16 v[202:205], v[158:161], v[214:217], v[202:205]
	s_addc_u32 s13, s13, 0
	s_waitcnt lgkmcnt(1)
	ds_read_b128 v[214:217], v242 offset:30048
	v_mfma_f32_16x16x32_f16 v[174:177], v[2:5], v[206:209], v[174:177]
	v_mfma_f32_16x16x32_f16 v[178:181], v[6:9], v[206:209], v[178:181]
	v_mfma_f32_16x16x32_f16 v[182:185], v[10:13], v[206:209], v[182:185]
	v_mfma_f32_16x16x32_f16 v[186:189], v[14:17], v[206:209], v[186:189]
	s_waitcnt lgkmcnt(1)
	ds_read_b128 v[206:209], v242 offset:29984
	v_mfma_f32_16x16x32_f16 v[174:177], v[18:21], v[210:213], v[174:177]
	v_mfma_f32_16x16x32_f16 v[178:181], v[22:25], v[210:213], v[178:181]
	v_mfma_f32_16x16x32_f16 v[182:185], v[26:29], v[210:213], v[182:185]
	v_mfma_f32_16x16x32_f16 v[186:189], v[30:33], v[210:213], v[186:189]
	s_waitcnt lgkmcnt(1)
	ds_read_b128 v[210:213], v242 offset:30000
	v_mfma_f32_16x16x32_f16 v[174:177], v[218:221], v[214:217], v[174:177]
	ds_read_b128 v[218:221], v255 offset:4096
	v_exp_f32_e32 v190, v190
	v_exp_f32_e32 v191, v191
	v_mfma_f32_16x16x32_f16 v[178:181], v[222:225], v[214:217], v[178:181]
	ds_read_b128 v[222:225], v255 offset:5120
	v_exp_f32_e32 v194, v194
	v_exp_f32_e32 v195, v195
	v_mfma_f32_16x16x32_f16 v[182:185], v[226:229], v[214:217], v[182:185]
	ds_read_b128 v[226:229], v255 offset:6144
	v_exp_f32_e32 v198, v198
	v_exp_f32_e32 v199, v199
	v_mfma_f32_16x16x32_f16 v[186:189], v[230:233], v[214:217], v[186:189]
	ds_read_b128 v[230:233], v255 offset:7168
	v_exp_f32_e32 v202, v202
	v_exp_f32_e32 v203, v203
	s_waitcnt lgkmcnt(5)
	ds_read_b128 v[214:217], v243 offset:16640
	v_mfma_f32_16x16x32_f16 v[174:177], v[34:37], v[206:209], v[174:177]
	v_add_f32_e32 v198, 1.0, v198
	v_add_f32_e32 v199, 1.0, v199
	v_mfma_f32_16x16x32_f16 v[178:181], v[38:41], v[206:209], v[178:181]
	v_add_f32_e32 v194, 1.0, v194
	v_add_f32_e32 v195, 1.0, v195
	v_mfma_f32_16x16x32_f16 v[182:185], v[42:45], v[206:209], v[182:185]
	v_fma_f32 v190, v190, v198, v198
	v_fma_f32 v191, v191, v199, v199
	v_mfma_f32_16x16x32_f16 v[186:189], v[46:49], v[206:209], v[186:189]
	v_rcp_f32_e32 v194, v194
	v_rcp_f32_e32 v195, v195
	v_fma_f32 v198, v198, v252, s16
	s_waitcnt lgkmcnt(5)
	ds_read_b128 v[206:209], v243 offset:16656
	v_mfma_f32_16x16x32_f16 v[174:177], v[50:53], v[210:213], v[174:177]
	v_fma_f32 v199, v199, v252, s16
	v_rcp_f32_e32 v190, v190
	v_mfma_f32_16x16x32_f16 v[178:181], v[54:57], v[210:213], v[178:181]
	v_rcp_f32_e32 v191, v191
	v_mul_f32_e32 v162, v162, v194
	v_mfma_f32_16x16x32_f16 v[182:185], v[58:61], v[210:213], v[182:185]
	v_mul_f32_e32 v163, v163, v195
	v_fma_f32 v162, v198, v190, v162
	v_mfma_f32_16x16x32_f16 v[186:189], v[62:65], v[210:213], v[186:189]
	v_fma_f32 v163, v199, v191, v163
	v_exp_f32_e32 v194, v162
	v_exp_f32_e32 v195, v163
	s_waitcnt lgkmcnt(1)
	ds_read_b128 v[210:213], v242 offset:30064
	v_mfma_f32_16x16x32_f16 v[174:177], v[98:101], v[214:217], v[174:177]
	v_add_f32_e32 v190, 1.0, v194
	v_add_f32_e32 v191, 1.0, v195
	v_mfma_f32_16x16x32_f16 v[178:181], v[102:105], v[214:217], v[178:181]
	v_add_f32_e32 v198, -1.0, v194
	v_add_f32_e32 v199, -1.0, v195
	v_mfma_f32_16x16x32_f16 v[182:185], v[106:109], v[214:217], v[182:185]
	v_fma_f32 v202, v202, v190, v190
	v_fma_f32 v203, v203, v191, v191
	v_mfma_f32_16x16x32_f16 v[186:189], v[110:113], v[214:217], v[186:189]
	v_rcp_f32_e32 v202, v202
	v_rcp_f32_e32 v203, v203
	v_mul_f32_e32 v202, v198, v202
	s_waitcnt lgkmcnt(1)
	ds_read_b128 v[214:217], v242 offset:30016
	v_mfma_f32_16x16x32_f16 v[174:177], v[114:117], v[206:209], v[174:177]
	v_mul_f32_e32 v203, v199, v203
	v_exp_f32_e32 v192, v192
	v_mfma_f32_16x16x32_f16 v[178:181], v[118:121], v[206:209], v[178:181]
	v_exp_f32_e32 v193, v193
	v_exp_f32_e32 v196, v196
	v_mfma_f32_16x16x32_f16 v[182:185], v[122:125], v[206:209], v[182:185]
	v_exp_f32_e32 v197, v197
	v_exp_f32_e32 v200, v200
	v_mfma_f32_16x16x32_f16 v[186:189], v[126:129], v[206:209], v[186:189]
	v_exp_f32_e32 v201, v201
	v_exp_f32_e32 v204, v204
	s_waitcnt lgkmcnt(1)
	ds_read_b128 v[206:209], v242 offset:30032
	v_mfma_f32_16x16x32_f16 v[174:177], v[218:221], v[210:213], v[174:177]
	ds_read_b128 v[218:221], v255 offset:0
	v_exp_f32_e32 v205, v205
	v_add_f32_e32 v200, 1.0, v200
	v_mfma_f32_16x16x32_f16 v[178:181], v[222:225], v[210:213], v[178:181]
	ds_read_b128 v[222:225], v255 offset:1024
	v_add_f32_e32 v201, 1.0, v201
	v_add_f32_e32 v196, 1.0, v196
	v_mfma_f32_16x16x32_f16 v[182:185], v[226:229], v[210:213], v[182:185]
	ds_read_b128 v[226:229], v255 offset:2048
	v_add_f32_e32 v197, 1.0, v197
	v_fma_f32 v192, v192, v200, v200
	v_mfma_f32_16x16x32_f16 v[186:189], v[230:233], v[210:213], v[186:189]
	ds_read_b128 v[230:233], v255 offset:3072
	v_fma_f32 v193, v193, v201, v201
	v_rcp_f32_e32 v196, v196
	v_rcp_f32_e32 v197, v197
	s_waitcnt lgkmcnt(5)
	ds_read_b128 v[210:213], v243 offset:16672
	v_mfma_f32_16x16x32_f16 v[174:177], v[66:69], v[214:217], v[174:177]
	v_fma_f32 v200, v200, v252, s16
	v_fma_f32 v201, v201, v252, s16
	v_mfma_f32_16x16x32_f16 v[178:181], v[70:73], v[214:217], v[178:181]
	v_rcp_f32_e32 v192, v192
	v_rcp_f32_e32 v193, v193
	v_mfma_f32_16x16x32_f16 v[182:185], v[74:77], v[214:217], v[182:185]
	v_mul_f32_e32 v164, v164, v196
	v_mul_f32_e32 v165, v165, v197
	v_mfma_f32_16x16x32_f16 v[186:189], v[78:81], v[214:217], v[186:189]
	v_fma_f32 v164, v200, v192, v164
	v_fma_f32 v165, v201, v193, v165
	v_exp_f32_e32 v196, v164
	s_waitcnt lgkmcnt(5)
	ds_read_b128 v[214:217], v243 offset:16688
	v_mfma_f32_16x16x32_f16 v[174:177], v[82:85], v[206:209], v[174:177]
	s_waitcnt vmcnt(0)
	ds_write_b128 v249, v[234:237] offset:27648
	ds_write_b128 v249, v[238:241] offset:2304
	global_load_dwordx4 v[234:237], v248, s[8:9]
	s_add_u32 s8, s8, 0x271000
	s_addc_u32 s9, s9, 0
	v_exp_f32_e32 v197, v165
	v_mfma_f32_16x16x32_f16 v[178:181], v[86:89], v[206:209], v[178:181]
	v_add_f32_e32 v192, 1.0, v196
	v_add_f32_e32 v193, 1.0, v197
	v_add_f32_e32 v200, -1.0, v196
	v_mfma_f32_16x16x32_f16 v[182:185], v[90:93], v[206:209], v[182:185]
	v_add_f32_e32 v201, -1.0, v197
	v_fma_f32 v204, v204, v192, v192
	v_mfma_f32_16x16x32_f16 v[186:189], v[94:97], v[206:209], v[186:189]
	v_fma_f32 v205, v205, v193, v193
	v_rcp_f32_e32 v204, v204
	v_rcp_f32_e32 v205, v205
	s_waitcnt lgkmcnt(3)
	ds_read_b128 v[206:209], v242 offset:32256
	v_mfma_f32_16x16x32_f16 v[174:177], v[130:133], v[210:213], v[174:177]
	v_mul_f32_e32 v204, v200, v204
	v_mul_f32_e32 v205, v201, v205
	v_mfma_f32_16x16x32_f16 v[178:181], v[134:137], v[210:213], v[178:181]
	v_cvt_pk_f16_f32 v202, v202, v203
	v_cvt_pk_f16_f32 v203, v204, v205
	v_mfma_f32_16x16x32_f16 v[182:185], v[138:141], v[210:213], v[182:185]
	ds_write_b64 v244, v[202:203] offset:0
	ds_read_b128 v[190:193], v245 offset:0
	v_mfma_f32_16x16x32_f16 v[186:189], v[142:145], v[210:213], v[186:189]
	ds_read_b128 v[194:197], v245 offset:512
	ds_read_b128 v[198:201], v245 offset:1024
	ds_read_b128 v[202:205], v245 offset:1536
	s_waitcnt lgkmcnt(8)
	ds_read_b128 v[210:213], v242 offset:32272
	v_mfma_f32_16x16x32_f16 v[174:177], v[146:149], v[214:217], v[174:177]
	v_mfma_f32_16x16x32_f16 v[178:181], v[150:153], v[214:217], v[178:181]
	v_mfma_f32_16x16x32_f16 v[182:185], v[154:157], v[214:217], v[182:185]
	v_mfma_f32_16x16x32_f16 v[186:189], v[158:161], v[214:217], v[186:189]
	s_waitcnt lgkmcnt(6)
	ds_read_b128 v[214:217], v242 offset:32352
	s_waitcnt lgkmcnt(5)
	v_mfma_f32_16x16x32_f16 v[190:193], v[2:5], v[206:209], v[190:193]
	s_waitcnt lgkmcnt(4)
	v_mfma_f32_16x16x32_f16 v[194:197], v[6:9], v[206:209], v[194:197]
	s_waitcnt lgkmcnt(3)
	v_mfma_f32_16x16x32_f16 v[198:201], v[10:13], v[206:209], v[198:201]
	s_waitcnt lgkmcnt(2)
	v_mfma_f32_16x16x32_f16 v[202:205], v[14:17], v[206:209], v[202:205]
	s_waitcnt lgkmcnt(1)
	ds_read_b128 v[206:209], v242 offset:32288
	v_mfma_f32_16x16x32_f16 v[190:193], v[18:21], v[210:213], v[190:193]
	v_mfma_f32_16x16x32_f16 v[194:197], v[22:25], v[210:213], v[194:197]
	v_mfma_f32_16x16x32_f16 v[198:201], v[26:29], v[210:213], v[198:201]
	v_mfma_f32_16x16x32_f16 v[202:205], v[30:33], v[210:213], v[202:205]
	s_waitcnt lgkmcnt(1)
	ds_read_b128 v[210:213], v242 offset:32304
	v_mfma_f32_16x16x32_f16 v[190:193], v[218:221], v[214:217], v[190:193]
	ds_read_b128 v[218:221], v255 offset:4096
	v_exp_f32_e32 v174, v174
	v_exp_f32_e32 v175, v175
	v_mfma_f32_16x16x32_f16 v[194:197], v[222:225], v[214:217], v[194:197]
	ds_read_b128 v[222:225], v255 offset:5120
	v_exp_f32_e32 v178, v178
	v_exp_f32_e32 v179, v179
	v_mfma_f32_16x16x32_f16 v[198:201], v[226:229], v[214:217], v[198:201]
	ds_read_b128 v[226:229], v255 offset:6144
	v_exp_f32_e32 v182, v182
	v_exp_f32_e32 v183, v183
	v_mfma_f32_16x16x32_f16 v[202:205], v[230:233], v[214:217], v[202:205]
	ds_read_b128 v[230:233], v255 offset:7168
	v_exp_f32_e32 v186, v186
	v_exp_f32_e32 v187, v187
	s_waitcnt lgkmcnt(5)
	ds_read_b128 v[214:217], v243 offset:17920
	v_mfma_f32_16x16x32_f16 v[190:193], v[34:37], v[206:209], v[190:193]
	v_add_f32_e32 v182, 1.0, v182
	v_add_f32_e32 v183, 1.0, v183
	v_mfma_f32_16x16x32_f16 v[194:197], v[38:41], v[206:209], v[194:197]
	v_add_f32_e32 v178, 1.0, v178
	v_add_f32_e32 v179, 1.0, v179
	v_mfma_f32_16x16x32_f16 v[198:201], v[42:45], v[206:209], v[198:201]
	v_fma_f32 v174, v174, v182, v182
	v_fma_f32 v175, v175, v183, v183
	v_mfma_f32_16x16x32_f16 v[202:205], v[46:49], v[206:209], v[202:205]
	v_rcp_f32_e32 v178, v178
	v_rcp_f32_e32 v179, v179
	v_fma_f32 v182, v182, v252, s16
	s_waitcnt lgkmcnt(5)
	ds_read_b128 v[206:209], v243 offset:17936
	v_mfma_f32_16x16x32_f16 v[190:193], v[50:53], v[210:213], v[190:193]
	v_fma_f32 v183, v183, v252, s16
	v_rcp_f32_e32 v174, v174
	v_mfma_f32_16x16x32_f16 v[194:197], v[54:57], v[210:213], v[194:197]
	v_rcp_f32_e32 v175, v175
	v_mul_f32_e32 v166, v166, v178
	v_mfma_f32_16x16x32_f16 v[198:201], v[58:61], v[210:213], v[198:201]
	v_mul_f32_e32 v167, v167, v179
	v_fma_f32 v166, v182, v174, v166
	v_mfma_f32_16x16x32_f16 v[202:205], v[62:65], v[210:213], v[202:205]
	v_fma_f32 v167, v183, v175, v167
	v_exp_f32_e32 v178, v166
	v_exp_f32_e32 v179, v167
	s_waitcnt lgkmcnt(1)
	ds_read_b128 v[210:213], v242 offset:32368
	v_mfma_f32_16x16x32_f16 v[190:193], v[98:101], v[214:217], v[190:193]
	v_add_f32_e32 v174, 1.0, v178
	v_add_f32_e32 v175, 1.0, v179
	v_mfma_f32_16x16x32_f16 v[194:197], v[102:105], v[214:217], v[194:197]
	v_add_f32_e32 v182, -1.0, v178
	v_add_f32_e32 v183, -1.0, v179
	v_mfma_f32_16x16x32_f16 v[198:201], v[106:109], v[214:217], v[198:201]
	v_fma_f32 v186, v186, v174, v174
	v_fma_f32 v187, v187, v175, v175
	v_mfma_f32_16x16x32_f16 v[202:205], v[110:113], v[214:217], v[202:205]
	v_rcp_f32_e32 v186, v186
	v_rcp_f32_e32 v187, v187
	v_mul_f32_e32 v186, v182, v186
	s_waitcnt lgkmcnt(1)
	ds_read_b128 v[214:217], v242 offset:32320
	v_mfma_f32_16x16x32_f16 v[190:193], v[114:117], v[206:209], v[190:193]
	v_mul_f32_e32 v187, v183, v187
	v_exp_f32_e32 v176, v176
	v_mfma_f32_16x16x32_f16 v[194:197], v[118:121], v[206:209], v[194:197]
	v_exp_f32_e32 v177, v177
	v_exp_f32_e32 v180, v180
	v_mfma_f32_16x16x32_f16 v[198:201], v[122:125], v[206:209], v[198:201]
	v_exp_f32_e32 v181, v181
	v_exp_f32_e32 v184, v184
	v_mfma_f32_16x16x32_f16 v[202:205], v[126:129], v[206:209], v[202:205]
	v_exp_f32_e32 v185, v185
	v_exp_f32_e32 v188, v188
	s_waitcnt lgkmcnt(1)
	ds_read_b128 v[206:209], v242 offset:32336
	v_mfma_f32_16x16x32_f16 v[190:193], v[218:221], v[210:213], v[190:193]
	ds_read_b128 v[218:221], v255 offset:0
	v_exp_f32_e32 v189, v189
	v_add_f32_e32 v184, 1.0, v184
	v_mfma_f32_16x16x32_f16 v[194:197], v[222:225], v[210:213], v[194:197]
	ds_read_b128 v[222:225], v255 offset:1024
	v_add_f32_e32 v185, 1.0, v185
	v_add_f32_e32 v180, 1.0, v180
	v_mfma_f32_16x16x32_f16 v[198:201], v[226:229], v[210:213], v[198:201]
	ds_read_b128 v[226:229], v255 offset:2048
	v_add_f32_e32 v181, 1.0, v181
	v_fma_f32 v176, v176, v184, v184
	v_mfma_f32_16x16x32_f16 v[202:205], v[230:233], v[210:213], v[202:205]
	ds_read_b128 v[230:233], v255 offset:3072
	v_fma_f32 v177, v177, v185, v185
	v_rcp_f32_e32 v180, v180
	v_rcp_f32_e32 v181, v181
	s_waitcnt lgkmcnt(5)
	ds_read_b128 v[210:213], v243 offset:17952
	v_mfma_f32_16x16x32_f16 v[190:193], v[66:69], v[214:217], v[190:193]
	v_fma_f32 v184, v184, v252, s16
	v_fma_f32 v185, v185, v252, s16
	v_mfma_f32_16x16x32_f16 v[194:197], v[70:73], v[214:217], v[194:197]
	v_rcp_f32_e32 v176, v176
	v_rcp_f32_e32 v177, v177
	v_mfma_f32_16x16x32_f16 v[198:201], v[74:77], v[214:217], v[198:201]
	v_mul_f32_e32 v168, v168, v180
	v_mul_f32_e32 v169, v169, v181
	v_mfma_f32_16x16x32_f16 v[202:205], v[78:81], v[214:217], v[202:205]
	v_fma_f32 v168, v184, v176, v168
	v_fma_f32 v169, v185, v177, v169
	v_exp_f32_e32 v180, v168
	s_waitcnt lgkmcnt(5)
	ds_read_b128 v[214:217], v243 offset:17968
	v_mfma_f32_16x16x32_f16 v[190:193], v[82:85], v[206:209], v[190:193]
	v_exp_f32_e32 v181, v169
	v_add_f32_e32 v176, 1.0, v180
	v_mfma_f32_16x16x32_f16 v[194:197], v[86:89], v[206:209], v[194:197]
	v_add_f32_e32 v177, 1.0, v181
	v_add_f32_e32 v184, -1.0, v180
	v_mfma_f32_16x16x32_f16 v[198:201], v[90:93], v[206:209], v[198:201]
	v_add_f32_e32 v185, -1.0, v181
	v_fma_f32 v188, v188, v176, v176
	v_mfma_f32_16x16x32_f16 v[202:205], v[94:97], v[206:209], v[202:205]
	v_fma_f32 v189, v189, v177, v177
	v_rcp_f32_e32 v188, v188
	v_rcp_f32_e32 v189, v189
	s_waitcnt lgkmcnt(1)
	ds_read_b128 v[206:209], v242 offset:0
	v_mfma_f32_16x16x32_f16 v[190:193], v[130:133], v[210:213], v[190:193]
	v_mul_f32_e32 v188, v184, v188
	v_mul_f32_e32 v189, v185, v189
	v_mfma_f32_16x16x32_f16 v[194:197], v[134:137], v[210:213], v[194:197]
	v_cvt_pk_f16_f32 v186, v186, v187
	v_cvt_pk_f16_f32 v187, v188, v189
	v_mfma_f32_16x16x32_f16 v[198:201], v[138:141], v[210:213], v[198:201]
	ds_write_b64 v244, v[186:187] offset:1280
	ds_read_b128 v[174:177], v245 offset:0
	v_mfma_f32_16x16x32_f16 v[202:205], v[142:145], v[210:213], v[202:205]
	ds_read_b128 v[178:181], v245 offset:512
	ds_read_b128 v[182:185], v245 offset:1024
	ds_read_b128 v[186:189], v245 offset:1536
	s_waitcnt lgkmcnt(6)
	ds_read_b128 v[210:213], v242 offset:96
	v_mfma_f32_16x16x32_f16 v[190:193], v[146:149], v[214:217], v[190:193]
	v_mfma_f32_16x16x32_f16 v[194:197], v[150:153], v[214:217], v[194:197]
	v_mfma_f32_16x16x32_f16 v[198:201], v[154:157], v[214:217], v[198:201]
	v_mfma_f32_16x16x32_f16 v[202:205], v[158:161], v[214:217], v[202:205]
	s_waitcnt vmcnt(0)
	ds_write_b128 v249, v[234:237] offset:4608
	s_waitcnt lgkmcnt(7)
	ds_read_b128 v[214:217], v242 offset:16
	s_waitcnt lgkmcnt(6)
	v_mfma_f32_16x16x32_f16 v[174:177], v[2:5], v[206:209], v[174:177]
	s_waitcnt lgkmcnt(5)
	v_mfma_f32_16x16x32_f16 v[178:181], v[6:9], v[206:209], v[178:181]
	s_waitcnt lgkmcnt(4)
	v_mfma_f32_16x16x32_f16 v[182:185], v[10:13], v[206:209], v[182:185]
	s_waitcnt lgkmcnt(3)
	v_mfma_f32_16x16x32_f16 v[186:189], v[14:17], v[206:209], v[186:189]
	s_waitcnt lgkmcnt(2)
	ds_read_b128 v[206:209], v242 offset:32
	v_mfma_f32_16x16x32_f16 v[174:177], v[218:221], v[210:213], v[174:177]
	ds_read_b128 v[218:221], v255 offset:4096
	v_exp_f32_e32 v190, v190
	v_exp_f32_e32 v191, v191
	v_exp_f32_e32 v194, v194
	v_mfma_f32_16x16x32_f16 v[178:181], v[222:225], v[210:213], v[178:181]
	ds_read_b128 v[222:225], v255 offset:5120
	v_exp_f32_e32 v195, v195
	v_exp_f32_e32 v198, v198
	v_exp_f32_e32 v199, v199
	v_exp_f32_e32 v202, v202
	v_mfma_f32_16x16x32_f16 v[182:185], v[226:229], v[210:213], v[182:185]
	ds_read_b128 v[226:229], v255 offset:6144
	v_exp_f32_e32 v203, v203
	v_add_f32_e32 v198, 1.0, v198
	v_add_f32_e32 v199, 1.0, v199
	v_add_f32_e32 v194, 1.0, v194
	v_mfma_f32_16x16x32_f16 v[186:189], v[230:233], v[210:213], v[186:189]
	ds_read_b128 v[230:233], v255 offset:7168
	v_add_f32_e32 v195, 1.0, v195
	v_fma_f32 v190, v190, v198, v198
	v_fma_f32 v191, v191, v199, v199
	v_rcp_f32_e32 v194, v194
	s_waitcnt lgkmcnt(5)
	ds_read_b128 v[210:213], v242 offset:112
	v_mfma_f32_16x16x32_f16 v[174:177], v[18:21], v[214:217], v[174:177]
	v_rcp_f32_e32 v195, v195
	v_fma_f32 v198, v198, v252, s16
	v_fma_f32 v199, v199, v252, s16
	v_rcp_f32_e32 v190, v190
	v_mfma_f32_16x16x32_f16 v[178:181], v[22:25], v[214:217], v[178:181]
	v_rcp_f32_e32 v191, v191
	v_mul_f32_e32 v170, v170, v194
	v_mul_f32_e32 v171, v171, v195
	v_fma_f32 v170, v198, v190, v170
	v_mfma_f32_16x16x32_f16 v[182:185], v[26:29], v[214:217], v[182:185]
	v_fma_f32 v171, v199, v191, v171
	v_exp_f32_e32 v194, v170
	v_exp_f32_e32 v195, v171
	v_add_f32_e32 v190, 1.0, v194
	v_mfma_f32_16x16x32_f16 v[186:189], v[30:33], v[214:217], v[186:189]
	v_add_f32_e32 v191, 1.0, v195
	v_add_f32_e32 v198, -1.0, v194
	v_add_f32_e32 v199, -1.0, v195
	v_fma_f32 v202, v202, v190, v190
	s_waitcnt lgkmcnt(5)
	ds_read_b128 v[214:217], v242 offset:48
	v_mfma_f32_16x16x32_f16 v[174:177], v[34:37], v[206:209], v[174:177]
	v_fma_f32 v203, v203, v191, v191
	v_rcp_f32_e32 v202, v202
	v_rcp_f32_e32 v203, v203
	v_mul_f32_e32 v202, v198, v202
	v_mfma_f32_16x16x32_f16 v[178:181], v[38:41], v[206:209], v[178:181]
	v_mul_f32_e32 v203, v199, v203
	v_exp_f32_e32 v192, v192
	v_exp_f32_e32 v193, v193
	v_exp_f32_e32 v196, v196
	v_mfma_f32_16x16x32_f16 v[182:185], v[42:45], v[206:209], v[182:185]
	v_exp_f32_e32 v197, v197
	v_exp_f32_e32 v200, v200
	v_exp_f32_e32 v201, v201
	v_exp_f32_e32 v204, v204
	v_mfma_f32_16x16x32_f16 v[186:189], v[46:49], v[206:209], v[186:189]
	v_exp_f32_e32 v205, v205
	v_add_f32_e32 v200, 1.0, v200
	v_add_f32_e32 v201, 1.0, v201
	v_add_f32_e32 v196, 1.0, v196
	s_waitcnt lgkmcnt(1)
	ds_read_b128 v[206:209], v242 offset:64
	v_mfma_f32_16x16x32_f16 v[174:177], v[218:221], v[210:213], v[174:177]
	ds_read_b128 v[218:221], v255 offset:0
	v_add_f32_e32 v197, 1.0, v197
	v_fma_f32 v192, v192, v200, v200
	v_fma_f32 v193, v193, v201, v201
	v_rcp_f32_e32 v196, v196
	v_mfma_f32_16x16x32_f16 v[178:181], v[222:225], v[210:213], v[178:181]
	ds_read_b128 v[222:225], v255 offset:1024
	v_rcp_f32_e32 v197, v197
	v_fma_f32 v200, v200, v252, s16
	v_fma_f32 v201, v201, v252, s16
	v_rcp_f32_e32 v192, v192
	v_mfma_f32_16x16x32_f16 v[182:185], v[226:229], v[210:213], v[182:185]
	ds_read_b128 v[226:229], v255 offset:2048
	v_rcp_f32_e32 v193, v193
	v_mul_f32_e32 v172, v172, v196
	v_mul_f32_e32 v173, v173, v197
	v_fma_f32 v172, v200, v192, v172
	v_mfma_f32_16x16x32_f16 v[186:189], v[230:233], v[210:213], v[186:189]
	ds_read_b128 v[230:233], v255 offset:3072
	v_fma_f32 v173, v201, v193, v173
	v_exp_f32_e32 v196, v172
	v_exp_f32_e32 v197, v173
	v_add_f32_e32 v192, 1.0, v196
	s_waitcnt lgkmcnt(5)
	ds_read_b128 v[210:213], v242 offset:80
	v_mfma_f32_16x16x32_f16 v[174:177], v[50:53], v[214:217], v[174:177]
	v_add_f32_e32 v193, 1.0, v197
	v_add_f32_e32 v200, -1.0, v196
	v_add_f32_e32 v201, -1.0, v197
	v_fma_f32 v204, v204, v192, v192
	v_mfma_f32_16x16x32_f16 v[178:181], v[54:57], v[214:217], v[178:181]
	v_fma_f32 v205, v205, v193, v193
	v_rcp_f32_e32 v204, v204
	v_rcp_f32_e32 v205, v205
	v_mul_f32_e32 v204, v200, v204
	v_mfma_f32_16x16x32_f16 v[182:185], v[58:61], v[214:217], v[182:185]
	v_mul_f32_e32 v205, v201, v205
	v_cvt_pk_f16_f32 v202, v202, v203
	v_cvt_pk_f16_f32 v203, v204, v205
	ds_write_b64 v244, v[202:203] offset:2560
	v_mfma_f32_16x16x32_f16 v[186:189], v[62:65], v[214:217], v[186:189]
	ds_read_b128 v[190:193], v245 offset:0
	ds_read_b128 v[194:197], v245 offset:512
	ds_read_b128 v[198:201], v245 offset:1024
	ds_read_b128 v[202:205], v245 offset:1536
	s_waitcnt lgkmcnt(0)
	s_barrier
	s_add_u32 s17, s17, 2
	s_cmp_lt_u32 s17, 16
	s_cbranch_scc1 .Llstm1_loop
	s_waitcnt lgkmcnt(0)
	ds_read_b128 v[234:237], v250
	s_mov_b64 exec, s[20:21]
	ds_read_b128 v[238:241], v250 offset:2560
	s_mov_b64 exec, -1
	s_waitcnt lgkmcnt(0)
	s_mov_b64 exec, s[18:19]
	global_store_dwordx4 v251, v[234:237], s[10:11]
	s_mov_b64 exec, s[20:21]
	global_store_dwordx4 v251, v[238:241], s[14:15]
	s_mov_b64 exec, -1
	s_branch .LBB6_39

	.amdhsa_kernel _Z6k_lstmILi256ELi10ELb1ELb0EEvPKDF16_S1_S1_PKfPDF16_S1_S1_S1_S3_S3_S3_PfS5_
		.amdhsa_group_segment_fixed_size 9216
		.amdhsa_private_segment_fixed_size 0
		.amdhsa_kernarg_size 104
		.amdhsa_user_sgpr_count 2
		.amdhsa_user_sgpr_dispatch_ptr 0
		.amdhsa_user_sgpr_queue_ptr 0
		.amdhsa_user_sgpr_kernarg_segment_ptr 1
		.amdhsa_user_sgpr_dispatch_id 0
		.amdhsa_user_sgpr_kernarg_preload_length 0
		.amdhsa_user_sgpr_kernarg_preload_offset 0
		.amdhsa_user_sgpr_private_segment_size 0
		.amdhsa_uses_dynamic_stack 0
		.amdhsa_enable_private_segment 0
		.amdhsa_system_sgpr_workgroup_id_x 1
		.amdhsa_system_sgpr_workgroup_id_y 0
		.amdhsa_system_sgpr_workgroup_id_z 0
		.amdhsa_system_sgpr_workgroup_info 0
		.amdhsa_system_vgpr_workitem_id 0
		.amdhsa_next_free_vgpr 256
		.amdhsa_next_free_sgpr 31
		.amdhsa_accum_offset 256
		.amdhsa_reserve_vcc 1
		.amdhsa_float_round_mode_32 0
		.amdhsa_float_round_mode_16_64 0
		.amdhsa_float_denorm_mode_32 3
		.amdhsa_float_denorm_mode_16_64 3
		.amdhsa_dx10_clamp 1
		.amdhsa_ieee_mode 1
		.amdhsa_fp16_overflow 0
		.amdhsa_tg_split 0
		.amdhsa_exception_fp_ieee_invalid_op 0
		.amdhsa_exception_fp_denorm_src 0
		.amdhsa_exception_fp_ieee_div_zero 0
		.amdhsa_exception_fp_ieee_overflow 0
		.amdhsa_exception_fp_ieee_underflow 0
		.amdhsa_exception_fp_ieee_inexact 0
		.amdhsa_exception_int_div_zero 0
	.end_amdhsa_kernel

_Z6k_lstmILi128ELi8ELb0ELb1EEvPKDF16_S1_S1_PKfPDF16_S1_S1_S1_S3_S3_S3_PfS5_:
	s_load_dwordx4 s[4:7], s[0:1], 0x10
	s_load_dwordx2 s[8:9], s[0:1], 0x0
	v_and_b32_e32 v1, 63, v0
	v_lshrrev_b32_e32 v205, 6, v0
	v_lshlrev_b32_e32 v206, 15, v205
	v_lshl_add_u32 v206, v1, 4, v206
	v_readfirstlane_b32 s24, v205
	s_waitcnt lgkmcnt(0)
	v_add_u32_e32 v1, 0x0, v206
	global_load_dwordx4 v[2:5], v1, s[4:5] offset:0
	global_load_dwordx4 v[6:9], v1, s[4:5] offset:1024
	global_load_dwordx4 v[10:13], v1, s[4:5] offset:2048
	global_load_dwordx4 v[14:17], v1, s[4:5] offset:3072
	v_add_u32_e32 v1, 0x1000, v206
	global_load_dwordx4 v[18:21], v1, s[4:5] offset:0
	global_load_dwordx4 v[22:25], v1, s[4:5] offset:1024
	global_load_dwordx4 v[26:29], v1, s[4:5] offset:2048
	global_load_dwordx4 v[30:33], v1, s[4:5] offset:3072
	v_add_u32_e32 v1, 0x2000, v206
	global_load_dwordx4 v[34:37], v1, s[4:5] offset:0
	global_load_dwordx4 v[38:41], v1, s[4:5] offset:1024
	global_load_dwordx4 v[42:45], v1, s[4:5] offset:2048
	global_load_dwordx4 v[46:49], v1, s[4:5] offset:3072
	v_add_u32_e32 v1, 0x3000, v206
	global_load_dwordx4 v[50:53], v1, s[4:5] offset:0
	global_load_dwordx4 v[54:57], v1, s[4:5] offset:1024
	global_load_dwordx4 v[58:61], v1, s[4:5] offset:2048
	global_load_dwordx4 v[62:65], v1, s[4:5] offset:3072
	v_add_u32_e32 v1, 0x4000, v206
	global_load_dwordx4 v[66:69], v1, s[4:5] offset:0
	global_load_dwordx4 v[70:73], v1, s[4:5] offset:1024
	global_load_dwordx4 v[74:77], v1, s[4:5] offset:2048
	global_load_dwordx4 v[78:81], v1, s[4:5] offset:3072
	v_add_u32_e32 v1, 0x5000, v206
	global_load_dwordx4 v[82:85], v1, s[4:5] offset:0
	global_load_dwordx4 v[86:89], v1, s[4:5] offset:1024
	global_load_dwordx4 v[90:93], v1, s[4:5] offset:2048
	global_load_dwordx4 v[94:97], v1, s[4:5] offset:3072
	v_add_u32_e32 v1, 0x6000, v206
	global_load_dwordx4 v[98:101], v1, s[4:5] offset:0
	global_load_dwordx4 v[102:105], v1, s[4:5] offset:1024
	global_load_dwordx4 v[106:109], v1, s[4:5] offset:2048
	global_load_dwordx4 v[110:113], v1, s[4:5] offset:3072
	v_add_u32_e32 v1, 0x7000, v206
	global_load_dwordx4 v[114:117], v1, s[4:5] offset:0
	global_load_dwordx4 v[118:121], v1, s[4:5] offset:1024
	global_load_dwordx4 v[122:125], v1, s[4:5] offset:2048
	global_load_dwordx4 v[126:129], v1, s[4:5] offset:3072
	v_lshlrev_b32_e32 v1, 2, v0
	global_load_dword v174, v1, s[6:7]
	v_add_u32_e32 v197, 0xf000, v1
	s_mul_i32 s22, s2, 48
	v_lshrrev_b32_e32 v1, 4, v0
	v_and_b32_e32 v205, 15, v0
	v_lshlrev_b32_e32 v205, 4, v205
	v_add_u32_e32 v206, s22, v1
	v_min_u32_e32 v198, 0x270f, v206
	v_lshl_add_u32 v198, v198, 8, v205
	v_add_u32_e32 v206, 16, v206
	v_min_u32_e32 v199, 0x270f, v206
	v_lshl_add_u32 v199, v199, 8, v205
	v_add_u32_e32 v206, 16, v206
	v_min_u32_e32 v200, 0x270f, v206
	v_lshl_add_u32 v200, v200, 8, v205
	v_mul_u32_u24_e32 v201, 0x50, v1
	v_and_b32_e32 v205, 3, v0
	v_mul_u32_u24_e32 v205, 0xf00, v205
	v_bfe_u32 v206, v0, 2, 2
	v_lshl_add_u32 v205, v206, 4, v205
	v_add_u32_e32 v201, v201, v205
	s_add_u32 s12, s8, 0x271000
	s_addc_u32 s13, s9, 0
	s_add_u32 s10, s8, 0x249f000
	s_addc_u32 s11, s9, 0
	global_load_dwordx4 v[186:189], v198, s[8:9]
	global_load_dwordx4 v[190:193], v199, s[8:9]
	global_load_dwordx4 v[178:181], v198, s[12:13]
	global_load_dwordx4 v[182:185], v198, s[10:11]
	global_load_dwordx4 v[142:145], v200, s[10:11]
	s_add_u32 s8, s8, 0x271000
	s_addc_u32 s9, s9, 0
	s_add_u32 s12, s12, 0x271000
	s_addc_u32 s13, s13, 0
	v_and_b32_e32 v1, 15, v0
	v_bfe_u32 v205, v0, 4, 2
	v_mul_u32_u24_e32 v194, 0x50, v1
	v_mul_u32_u24_e32 v206, 0xf00, v205
	v_add_u32_e32 v194, v194, v206
	v_add_u32_e32 v195, 0x7800, v194
	v_add_u32_e32 v207, 0xf800, v194
	v_lshrrev_b32_e32 v206, 6, v0
	v_lshrrev_b32_e32 v196, 1, v205
	v_and_b32_e32 v204, 1, v206
	v_lshl_add_u32 v196, v204, 1, v196
	v_mul_u32_u24_e32 v196, 0xf00, v196
	v_mul_u32_u24_e32 v204, 0x50, v1
	v_add_u32_e32 v196, v196, v204
	v_add_u32_e32 v196, 0x7800, v196
	v_lshrrev_b32_e32 v204, 1, v206
	v_lshl_add_u32 v196, v204, 4, v196
	v_and_b32_e32 v204, 1, v205
	v_lshl_add_u32 v196, v204, 3, v196
	v_lshl_add_u32 v208, v206, 2, v205
	v_lshlrev_b32_e32 v208, 2, v208
	v_lshl_add_u32 v208, v1, 7, v208
	v_add_u32_e32 v208, 0x13400, v208
	v_mov_b32_e32 v158, 0
	v_mov_b32_e32 v159, 0
	v_mov_b32_e32 v160, 0
	v_mov_b32_e32 v161, 0
	v_mov_b32_e32 v130, 0
	v_mov_b32_e32 v131, 0
	v_mov_b32_e32 v132, 0
	v_mov_b32_e32 v133, 0
	v_mov_b32_e32 v134, 0
	v_mov_b32_e32 v135, 0
	v_mov_b32_e32 v136, 0
	v_mov_b32_e32 v137, 0
	v_mov_b32_e32 v138, 0
	v_mov_b32_e32 v139, 0
	v_mov_b32_e32 v140, 0
	v_mov_b32_e32 v141, 0
	v_mov_b32_e32 v204, 0x4038aa3b
	s_mov_b32 s16, 0xc0b8aa3b
	v_lshlrev_b32_e32 v1, 4, v0
	v_add_u32_e32 v1, 0x7800, v1
	ds_write_b128 v1, v[158:161]
	ds_write_b128 v1, v[158:161] offset:8192
	s_waitcnt vmcnt(0)
	ds_write_b32 v197, v174
	ds_write_b128 v201, v[190:193] offset:1280
	ds_write_b128 v201, v[182:185] offset:63488
	s_cmp_ge_u32 s24, 4
	s_cbranch_scc1 .Ll2_pro_skip
	ds_write_b128 v201, v[186:189]
	ds_write_b128 v201, v[178:181] offset:15360
	v_add_u32_e32 v1, 0xa00, v201
	ds_write_b128 v1, v[142:145] offset:63488
.Ll2_pro_skip:
	v_lshrrev_b32_e32 v206, 6, v0
	v_lshlrev_b32_e32 v197, 6, v206
	v_lshl_add_u32 v197, v205, 4, v197
	v_add_u32_e32 v197, 0xf000, v197
	s_waitcnt lgkmcnt(0)
	s_barrier
	ds_read_b128 v[142:145], v197 offset:0
	ds_read_b128 v[146:149], v197 offset:512
	ds_read_b128 v[150:153], v197 offset:1024
	ds_read_b128 v[154:157], v197 offset:1536
	ds_read_b128 v[174:177], v194 offset:0
	ds_read_b128 v[178:181], v194 offset:16
	s_waitcnt lgkmcnt(1)
	ds_read_b128 v[182:185], v194 offset:32
	v_mfma_f32_16x16x32_f16 v[142:145], v[2:5], v[174:177], v[142:145]
	v_mfma_f32_16x16x32_f16 v[146:149], v[6:9], v[174:177], v[146:149]
	v_mfma_f32_16x16x32_f16 v[150:153], v[10:13], v[174:177], v[150:153]
	v_mfma_f32_16x16x32_f16 v[154:157], v[14:17], v[174:177], v[154:157]
	s_waitcnt lgkmcnt(1)
	ds_read_b128 v[174:177], v194 offset:48
	v_mfma_f32_16x16x32_f16 v[142:145], v[18:21], v[178:181], v[142:145]
	ds_read_b128 v[158:161], v197 offset:0
	v_mfma_f32_16x16x32_f16 v[146:149], v[22:25], v[178:181], v[146:149]
	ds_read_b128 v[162:165], v197 offset:512
	v_mfma_f32_16x16x32_f16 v[150:153], v[26:29], v[178:181], v[150:153]
	ds_read_b128 v[166:169], v197 offset:1024
	v_mfma_f32_16x16x32_f16 v[154:157], v[30:33], v[178:181], v[154:157]
	ds_read_b128 v[170:173], v197 offset:1536
	s_waitcnt lgkmcnt(0)
	s_mov_b32 s17, 0
	s_barrier
.Llstm2_loop:
	ds_read_b128 v[178:181], v195 offset:0
	v_mfma_f32_16x16x32_f16 v[142:145], v[34:37], v[182:185], v[142:145]
	v_mfma_f32_16x16x32_f16 v[146:149], v[38:41], v[182:185], v[146:149]
	v_mfma_f32_16x16x32_f16 v[150:153], v[42:45], v[182:185], v[150:153]
	v_mfma_f32_16x16x32_f16 v[154:157], v[46:49], v[182:185], v[154:157]
	ds_read_b128 v[182:185], v195 offset:16
	v_mfma_f32_16x16x32_f16 v[142:145], v[50:53], v[174:177], v[142:145]
	v_mfma_f32_16x16x32_f16 v[146:149], v[54:57], v[174:177], v[146:149]
	v_mfma_f32_16x16x32_f16 v[150:153], v[58:61], v[174:177], v[150:153]
	v_mfma_f32_16x16x32_f16 v[154:157], v[62:65], v[174:177], v[154:157]
	s_cmp_ge_u32 s24, 4
	s_cbranch_scc1 .Lskipx51
	global_load_dwordx4 v[186:189], v198, s[12:13]
.Lskipx51:
	s_waitcnt lgkmcnt(1)
	ds_read_b128 v[174:177], v195 offset:32
	v_mfma_f32_16x16x32_f16 v[142:145], v[66:69], v[178:181], v[142:145]
	v_mfma_f32_16x16x32_f16 v[146:149], v[70:73], v[178:181], v[146:149]
	v_mfma_f32_16x16x32_f16 v[150:153], v[74:77], v[178:181], v[150:153]
	v_mfma_f32_16x16x32_f16 v[154:157], v[78:81], v[178:181], v[154:157]
	global_load_dwordx4 v[190:193], v199, s[8:9]
	s_waitcnt lgkmcnt(1)
	ds_read_b128 v[178:181], v195 offset:48
	v_mfma_f32_16x16x32_f16 v[142:145], v[82:85], v[182:185], v[142:145]
	v_mfma_f32_16x16x32_f16 v[146:149], v[86:89], v[182:185], v[146:149]
	v_mfma_f32_16x16x32_f16 v[150:153], v[90:93], v[182:185], v[150:153]
	v_mfma_f32_16x16x32_f16 v[154:157], v[94:97], v[182:185], v[154:157]
	s_add_u32 s12, s12, 0x271000
	s_waitcnt lgkmcnt(1)
	ds_read_b128 v[182:185], v194 offset:1280
	v_mfma_f32_16x16x32_f16 v[142:145], v[98:101], v[174:177], v[142:145]
	v_mfma_f32_16x16x32_f16 v[146:149], v[102:105], v[174:177], v[146:149]
	v_mfma_f32_16x16x32_f16 v[150:153], v[106:109], v[174:177], v[150:153]
	v_mfma_f32_16x16x32_f16 v[154:157], v[110:113], v[174:177], v[154:157]
	s_addc_u32 s13, s13, 0
	s_waitcnt lgkmcnt(1)
	ds_read_b128 v[174:177], v194 offset:1296
	v_mfma_f32_16x16x32_f16 v[142:145], v[114:117], v[178:181], v[142:145]
	v_mfma_f32_16x16x32_f16 v[146:149], v[118:121], v[178:181], v[146:149]
	s_add_u32 s8, s8, 0x271000
	v_mfma_f32_16x16x32_f16 v[150:153], v[122:125], v[178:181], v[150:153]
	v_mfma_f32_16x16x32_f16 v[154:157], v[126:129], v[178:181], v[154:157]
	s_addc_u32 s9, s9, 0
	s_waitcnt lgkmcnt(1)
	ds_read_b128 v[178:181], v195 offset:1280
	v_mfma_f32_16x16x32_f16 v[158:161], v[2:5], v[182:185], v[158:161]
	v_mfma_f32_16x16x32_f16 v[162:165], v[6:9], v[182:185], v[162:165]
	v_mfma_f32_16x16x32_f16 v[166:169], v[10:13], v[182:185], v[166:169]
	v_mfma_f32_16x16x32_f16 v[170:173], v[14:17], v[182:185], v[170:173]
	s_waitcnt lgkmcnt(1)
	ds_read_b128 v[182:185], v195 offset:1296
	v_mfma_f32_16x16x32_f16 v[158:161], v[18:21], v[174:177], v[158:161]
	v_mfma_f32_16x16x32_f16 v[162:165], v[22:25], v[174:177], v[162:165]
	v_mfma_f32_16x16x32_f16 v[166:169], v[26:29], v[174:177], v[166:169]
	v_mfma_f32_16x16x32_f16 v[170:173], v[30:33], v[174:177], v[170:173]
	s_waitcnt lgkmcnt(1)
	ds_read_b128 v[174:177], v194 offset:1312
	v_mfma_f32_16x16x32_f16 v[158:161], v[66:69], v[178:181], v[158:161]
	v_exp_f32_e32 v142, v142
	v_exp_f32_e32 v143, v143
	v_exp_f32_e32 v146, v146
	v_mfma_f32_16x16x32_f16 v[162:165], v[70:73], v[178:181], v[162:165]
	v_exp_f32_e32 v147, v147
	v_exp_f32_e32 v150, v150
	v_exp_f32_e32 v151, v151
	v_exp_f32_e32 v154, v154
	v_mfma_f32_16x16x32_f16 v[166:169], v[74:77], v[178:181], v[166:169]
	v_exp_f32_e32 v155, v155
	v_add_f32_e32 v150, 1.0, v150
	v_add_f32_e32 v151, 1.0, v151
	v_add_f32_e32 v146, 1.0, v146
	v_mfma_f32_16x16x32_f16 v[170:173], v[78:81], v[178:181], v[170:173]
	v_add_f32_e32 v147, 1.0, v147
	v_fma_f32 v142, v142, v150, v150
	v_fma_f32 v143, v143, v151, v151
	v_rcp_f32_e32 v146, v146
	s_waitcnt lgkmcnt(1)
	ds_read_b128 v[178:181], v194 offset:1328
	v_mfma_f32_16x16x32_f16 v[158:161], v[82:85], v[182:185], v[158:161]
	v_rcp_f32_e32 v147, v147
	v_fma_f32 v150, v150, v204, s16
	v_fma_f32 v151, v151, v204, s16
	v_rcp_f32_e32 v142, v142
	v_mfma_f32_16x16x32_f16 v[162:165], v[86:89], v[182:185], v[162:165]
	v_rcp_f32_e32 v143, v143
	v_mul_f32_e32 v130, v130, v146
	v_mul_f32_e32 v131, v131, v147
	v_fma_f32 v130, v150, v142, v130
	v_mfma_f32_16x16x32_f16 v[166:169], v[90:93], v[182:185], v[166:169]
	v_fma_f32 v131, v151, v143, v131
	v_exp_f32_e32 v146, v130
	v_exp_f32_e32 v147, v131
	v_add_f32_e32 v142, 1.0, v146
	v_mfma_f32_16x16x32_f16 v[170:173], v[94:97], v[182:185], v[170:173]
	v_add_f32_e32 v143, 1.0, v147
	v_add_f32_e32 v150, -1.0, v146
	v_add_f32_e32 v151, -1.0, v147
	v_fma_f32 v154, v154, v142, v142
	s_waitcnt lgkmcnt(1)
	ds_read_b128 v[182:185], v195 offset:1312
	v_mfma_f32_16x16x32_f16 v[158:161], v[34:37], v[174:177], v[158:161]
	v_fma_f32 v155, v155, v143, v143
	v_rcp_f32_e32 v154, v154
	v_rcp_f32_e32 v155, v155
	v_mul_f32_e32 v154, v150, v154
	v_mfma_f32_16x16x32_f16 v[162:165], v[38:41], v[174:177], v[162:165]
	v_mul_f32_e32 v155, v151, v155
	v_exp_f32_e32 v144, v144
	v_exp_f32_e32 v145, v145
	v_exp_f32_e32 v148, v148
	v_mfma_f32_16x16x32_f16 v[166:169], v[42:45], v[174:177], v[166:169]
	v_exp_f32_e32 v149, v149
	v_exp_f32_e32 v152, v152
	v_exp_f32_e32 v153, v153
	v_exp_f32_e32 v156, v156
	v_mfma_f32_16x16x32_f16 v[170:173], v[46:49], v[174:177], v[170:173]
	v_exp_f32_e32 v157, v157
	v_add_f32_e32 v152, 1.0, v152
	v_add_f32_e32 v153, 1.0, v153
	v_add_f32_e32 v148, 1.0, v148
	s_waitcnt lgkmcnt(1)
	ds_read_b128 v[174:177], v195 offset:1328
	v_mfma_f32_16x16x32_f16 v[158:161], v[50:53], v[178:181], v[158:161]
	s_waitcnt vmcnt(0)
	s_cmp_ge_u32 s24, 4
	s_cbranch_scc1 .Lskips52
	ds_write_b128 v201, v[186:189] offset:0
.Lskips52:
	ds_write_b128 v201, v[190:193] offset:16640
	v_add_f32_e32 v149, 1.0, v149
	v_fma_f32 v144, v144, v152, v152
	v_fma_f32 v145, v145, v153, v153
	v_mfma_f32_16x16x32_f16 v[162:165], v[54:57], v[178:181], v[162:165]
	v_rcp_f32_e32 v148, v148
	v_rcp_f32_e32 v149, v149
	v_fma_f32 v152, v152, v204, s16
	v_fma_f32 v153, v153, v204, s16
	v_mfma_f32_16x16x32_f16 v[166:169], v[58:61], v[178:181], v[166:169]
	v_rcp_f32_e32 v144, v144
	v_rcp_f32_e32 v145, v145
	v_mul_f32_e32 v132, v132, v148
	v_mul_f32_e32 v133, v133, v149
	v_mfma_f32_16x16x32_f16 v[170:173], v[62:65], v[178:181], v[170:173]
	v_fma_f32 v132, v152, v144, v132
	v_fma_f32 v133, v153, v145, v133
	v_exp_f32_e32 v148, v132
	v_exp_f32_e32 v149, v133
	v_add_f32_e32 v144, 1.0, v148
	s_waitcnt lgkmcnt(3)
	ds_read_b128 v[178:181], v194 offset:2560
	v_mfma_f32_16x16x32_f16 v[158:161], v[98:101], v[182:185], v[158:161]
	v_add_f32_e32 v145, 1.0, v149
	v_add_f32_e32 v152, -1.0, v148
	v_add_f32_e32 v153, -1.0, v149
	v_fma_f32 v156, v156, v144, v144
	v_mfma_f32_16x16x32_f16 v[162:165], v[102:105], v[182:185], v[162:165]
	v_fma_f32 v157, v157, v145, v145
	v_rcp_f32_e32 v156, v156
	v_rcp_f32_e32 v157, v157
	v_mul_f32_e32 v156, v152, v156
	v_mfma_f32_16x16x32_f16 v[166:169], v[106:109], v[182:185], v[166:169]
	v_mul_f32_e32 v157, v153, v157
	v_cvt_pk_f16_f32 v154, v154, v155
	v_cvt_pk_f16_f32 v155, v156, v157
	ds_write_b64 v196, v[154:155] offset:15360
	v_mfma_f32_16x16x32_f16 v[170:173], v[110:113], v[182:185], v[170:173]
	ds_read_b128 v[142:145], v197 offset:0
	ds_read_b128 v[146:149], v197 offset:512
	ds_read_b128 v[150:153], v197 offset:1024
	ds_read_b128 v[154:157], v197 offset:1536
	s_waitcnt lgkmcnt(8)
	ds_read_b128 v[182:185], v194 offset:2576
	v_mfma_f32_16x16x32_f16 v[158:161], v[114:117], v[174:177], v[158:161]
	v_mfma_f32_16x16x32_f16 v[162:165], v[118:121], v[174:177], v[162:165]
	v_mfma_f32_16x16x32_f16 v[166:169], v[122:125], v[174:177], v[166:169]
	v_mfma_f32_16x16x32_f16 v[170:173], v[126:129], v[174:177], v[170:173]
	s_waitcnt lgkmcnt(6)
	ds_read_b128 v[174:177], v195 offset:2560
	s_waitcnt lgkmcnt(5)
	v_mfma_f32_16x16x32_f16 v[142:145], v[2:5], v[178:181], v[142:145]
	s_waitcnt lgkmcnt(4)
	v_mfma_f32_16x16x32_f16 v[146:149], v[6:9], v[178:181], v[146:149]
	s_waitcnt lgkmcnt(3)
	v_mfma_f32_16x16x32_f16 v[150:153], v[10:13], v[178:181], v[150:153]
	s_waitcnt lgkmcnt(2)
	v_mfma_f32_16x16x32_f16 v[154:157], v[14:17], v[178:181], v[154:157]
	s_waitcnt lgkmcnt(1)
	ds_read_b128 v[178:181], v195 offset:2576
	v_mfma_f32_16x16x32_f16 v[142:145], v[18:21], v[182:185], v[142:145]
	v_mfma_f32_16x16x32_f16 v[146:149], v[22:25], v[182:185], v[146:149]
	v_mfma_f32_16x16x32_f16 v[150:153], v[26:29], v[182:185], v[150:153]
	v_mfma_f32_16x16x32_f16 v[154:157], v[30:33], v[182:185], v[154:157]
	s_waitcnt lgkmcnt(1)
	ds_read_b128 v[182:185], v194 offset:2592
	v_mfma_f32_16x16x32_f16 v[142:145], v[66:69], v[174:177], v[142:145]
	v_exp_f32_e32 v158, v158
	v_exp_f32_e32 v159, v159
	v_exp_f32_e32 v162, v162
	v_mfma_f32_16x16x32_f16 v[146:149], v[70:73], v[174:177], v[146:149]
	v_exp_f32_e32 v163, v163
	v_exp_f32_e32 v166, v166
	v_exp_f32_e32 v167, v167
	v_exp_f32_e32 v170, v170
	v_mfma_f32_16x16x32_f16 v[150:153], v[74:77], v[174:177], v[150:153]
	v_exp_f32_e32 v171, v171
	v_add_f32_e32 v166, 1.0, v166
	v_add_f32_e32 v167, 1.0, v167
	v_add_f32_e32 v162, 1.0, v162
	v_mfma_f32_16x16x32_f16 v[154:157], v[78:81], v[174:177], v[154:157]
	v_add_f32_e32 v163, 1.0, v163
	v_fma_f32 v158, v158, v166, v166
	v_fma_f32 v159, v159, v167, v167
	v_rcp_f32_e32 v162, v162
	s_waitcnt lgkmcnt(1)
	ds_read_b128 v[174:177], v194 offset:2608
	v_mfma_f32_16x16x32_f16 v[142:145], v[82:85], v[178:181], v[142:145]
	v_rcp_f32_e32 v163, v163
	v_fma_f32 v166, v166, v204, s16
	v_fma_f32 v167, v167, v204, s16
	v_rcp_f32_e32 v158, v158
	v_mfma_f32_16x16x32_f16 v[146:149], v[86:89], v[178:181], v[146:149]
	v_rcp_f32_e32 v159, v159
	v_mul_f32_e32 v134, v134, v162
	v_mul_f32_e32 v135, v135, v163
	v_fma_f32 v134, v166, v158, v134
	v_mfma_f32_16x16x32_f16 v[150:153], v[90:93], v[178:181], v[150:153]
	v_fma_f32 v135, v167, v159, v135
	v_exp_f32_e32 v162, v134
	v_exp_f32_e32 v163, v135
	v_add_f32_e32 v158, 1.0, v162
	v_mfma_f32_16x16x32_f16 v[154:157], v[94:97], v[178:181], v[154:157]
	v_add_f32_e32 v159, 1.0, v163
	v_add_f32_e32 v166, -1.0, v162
	v_add_f32_e32 v167, -1.0, v163
	v_fma_f32 v170, v170, v158, v158
	s_waitcnt lgkmcnt(1)
	ds_read_b128 v[178:181], v195 offset:2592
	v_mfma_f32_16x16x32_f16 v[142:145], v[34:37], v[182:185], v[142:145]
	v_fma_f32 v171, v171, v159, v159
	v_rcp_f32_e32 v170, v170
	v_rcp_f32_e32 v171, v171
	v_mul_f32_e32 v170, v166, v170
	v_mfma_f32_16x16x32_f16 v[146:149], v[38:41], v[182:185], v[146:149]
	v_mul_f32_e32 v171, v167, v171
	v_exp_f32_e32 v160, v160
	v_exp_f32_e32 v161, v161
	v_exp_f32_e32 v164, v164
	v_mfma_f32_16x16x32_f16 v[150:153], v[42:45], v[182:185], v[150:153]
	v_exp_f32_e32 v165, v165
	v_exp_f32_e32 v168, v168
	v_exp_f32_e32 v169, v169
	v_exp_f32_e32 v172, v172
	v_mfma_f32_16x16x32_f16 v[154:157], v[46:49], v[182:185], v[154:157]
	v_exp_f32_e32 v173, v173
	v_add_f32_e32 v168, 1.0, v168
	v_add_f32_e32 v169, 1.0, v169
	v_add_f32_e32 v164, 1.0, v164
	s_waitcnt lgkmcnt(1)
	ds_read_b128 v[182:185], v195 offset:2608
	v_mfma_f32_16x16x32_f16 v[142:145], v[50:53], v[174:177], v[142:145]
	v_add_f32_e32 v165, 1.0, v165
	v_fma_f32 v160, v160, v168, v168
	v_fma_f32 v161, v161, v169, v169
	v_rcp_f32_e32 v164, v164
	v_mfma_f32_16x16x32_f16 v[146:149], v[54:57], v[174:177], v[146:149]
	v_rcp_f32_e32 v165, v165
	v_fma_f32 v168, v168, v204, s16
	v_fma_f32 v169, v169, v204, s16
	v_rcp_f32_e32 v160, v160
	v_mfma_f32_16x16x32_f16 v[150:153], v[58:61], v[174:177], v[150:153]
	v_rcp_f32_e32 v161, v161
	v_mul_f32_e32 v136, v136, v164
	v_mul_f32_e32 v137, v137, v165
	v_fma_f32 v136, v168, v160, v136
	v_mfma_f32_16x16x32_f16 v[154:157], v[62:65], v[174:177], v[154:157]
	v_fma_f32 v137, v169, v161, v137
	v_exp_f32_e32 v164, v136
	v_exp_f32_e32 v165, v137
	v_add_f32_e32 v160, 1.0, v164
	s_waitcnt lgkmcnt(1)
	ds_read_b128 v[174:177], v194 offset:15360
	v_mfma_f32_16x16x32_f16 v[142:145], v[98:101], v[178:181], v[142:145]
	v_add_f32_e32 v161, 1.0, v165
	v_add_f32_e32 v168, -1.0, v164
	v_add_f32_e32 v169, -1.0, v165
	v_fma_f32 v172, v172, v160, v160
	v_mfma_f32_16x16x32_f16 v[146:149], v[102:105], v[178:181], v[146:149]
	v_fma_f32 v173, v173, v161, v161
	v_rcp_f32_e32 v172, v172
	v_rcp_f32_e32 v173, v173
	v_mul_f32_e32 v172, v168, v172
	v_mfma_f32_16x16x32_f16 v[150:153], v[106:109], v[178:181], v[150:153]
	v_mul_f32_e32 v173, v169, v173
	v_cvt_pk_f16_f32 v170, v170, v171
	v_cvt_pk_f16_f32 v171, v172, v173
	ds_write_b64 v196, v[170:171] offset:16640
	v_mfma_f32_16x16x32_f16 v[154:157], v[110:113], v[178:181], v[154:157]
	ds_read_b128 v[158:161], v197 offset:0
	ds_read_b128 v[162:165], v197 offset:512
	ds_read_b128 v[166:169], v197 offset:1024
	ds_read_b128 v[170:173], v197 offset:1536
	s_waitcnt lgkmcnt(6)
	ds_read_b128 v[178:181], v194 offset:15376
	v_mfma_f32_16x16x32_f16 v[142:145], v[114:117], v[182:185], v[142:145]
	v_mfma_f32_16x16x32_f16 v[146:149], v[118:121], v[182:185], v[146:149]
	v_mfma_f32_16x16x32_f16 v[150:153], v[122:125], v[182:185], v[150:153]
	v_mfma_f32_16x16x32_f16 v[154:157], v[126:129], v[182:185], v[154:157]
	s_waitcnt lgkmcnt(6)
	ds_read_b128 v[182:185], v194 offset:15392
	s_waitcnt lgkmcnt(5)
	v_mfma_f32_16x16x32_f16 v[158:161], v[2:5], v[174:177], v[158:161]
	s_waitcnt lgkmcnt(4)
	v_mfma_f32_16x16x32_f16 v[162:165], v[6:9], v[174:177], v[162:165]
	s_waitcnt lgkmcnt(3)
	v_mfma_f32_16x16x32_f16 v[166:169], v[10:13], v[174:177], v[166:169]
	s_waitcnt lgkmcnt(2)
	v_mfma_f32_16x16x32_f16 v[170:173], v[14:17], v[174:177], v[170:173]
	s_waitcnt lgkmcnt(1)
	ds_read_b128 v[174:177], v194 offset:15408
	v_mfma_f32_16x16x32_f16 v[158:161], v[18:21], v[178:181], v[158:161]
	v_exp_f32_e32 v142, v142
	v_exp_f32_e32 v143, v143
	v_exp_f32_e32 v146, v146
	v_exp_f32_e32 v147, v147
	v_exp_f32_e32 v150, v150
	v_exp_f32_e32 v151, v151
	v_exp_f32_e32 v154, v154
	v_exp_f32_e32 v155, v155
	v_add_f32_e32 v150, 1.0, v150
	v_add_f32_e32 v151, 1.0, v151
	v_add_f32_e32 v146, 1.0, v146
	v_add_f32_e32 v147, 1.0, v147
	v_fma_f32 v142, v142, v150, v150
	v_fma_f32 v143, v143, v151, v151
	v_rcp_f32_e32 v146, v146
	v_rcp_f32_e32 v147, v147
	v_fma_f32 v150, v150, v204, s16
	v_fma_f32 v151, v151, v204, s16
	v_rcp_f32_e32 v142, v142
	v_mfma_f32_16x16x32_f16 v[162:165], v[22:25], v[178:181], v[162:165]
	v_rcp_f32_e32 v143, v143
	v_mul_f32_e32 v138, v138, v146
	v_mul_f32_e32 v139, v139, v147
	v_fma_f32 v138, v150, v142, v138
	v_fma_f32 v139, v151, v143, v139
	v_exp_f32_e32 v146, v138
	v_exp_f32_e32 v147, v139
	v_add_f32_e32 v142, 1.0, v146
	v_add_f32_e32 v143, 1.0, v147
	v_add_f32_e32 v150, -1.0, v146
	v_add_f32_e32 v151, -1.0, v147
	v_fma_f32 v154, v154, v142, v142
	v_fma_f32 v155, v155, v143, v143
	v_rcp_f32_e32 v154, v154
	v_rcp_f32_e32 v155, v155
	v_mul_f32_e32 v154, v150, v154
	v_mul_f32_e32 v155, v151, v155
	v_exp_f32_e32 v144, v144
	v_exp_f32_e32 v145, v145
	v_exp_f32_e32 v148, v148
	v_mfma_f32_16x16x32_f16 v[166:169], v[26:29], v[178:181], v[166:169]
	v_exp_f32_e32 v149, v149
	v_exp_f32_e32 v152, v152
	v_exp_f32_e32 v153, v153
	v_exp_f32_e32 v156, v156
	v_exp_f32_e32 v157, v157
	v_add_f32_e32 v152, 1.0, v152
	v_add_f32_e32 v153, 1.0, v153
	v_add_f32_e32 v148, 1.0, v148
	v_add_f32_e32 v149, 1.0, v149
	v_fma_f32 v144, v144, v152, v152
	v_fma_f32 v145, v145, v153, v153
	v_rcp_f32_e32 v148, v148
	v_rcp_f32_e32 v149, v149
	v_fma_f32 v152, v152, v204, s16
	v_fma_f32 v153, v153, v204, s16
	v_rcp_f32_e32 v144, v144
	v_rcp_f32_e32 v145, v145
	v_mul_f32_e32 v140, v140, v148
	v_mul_f32_e32 v141, v141, v149
	v_fma_f32 v140, v152, v144, v140
	v_mfma_f32_16x16x32_f16 v[170:173], v[30:33], v[178:181], v[170:173]
	v_fma_f32 v141, v153, v145, v141
	v_exp_f32_e32 v148, v140
	v_exp_f32_e32 v149, v141
	v_add_f32_e32 v144, 1.0, v148
	v_add_f32_e32 v145, 1.0, v149
	v_add_f32_e32 v152, -1.0, v148
	v_add_f32_e32 v153, -1.0, v149
	v_fma_f32 v156, v156, v144, v144
	v_fma_f32 v157, v157, v145, v145
	v_rcp_f32_e32 v156, v156
	v_rcp_f32_e32 v157, v157
	v_mul_f32_e32 v156, v152, v156
	v_mul_f32_e32 v157, v153, v157
	v_cvt_pk_f16_f32 v154, v154, v155
	v_cvt_pk_f16_f32 v155, v156, v157
	ds_write_b64 v196, v[154:155] offset:17920
	ds_read_b128 v[142:145], v197 offset:0
	ds_read_b128 v[146:149], v197 offset:512
	ds_read_b128 v[150:153], v197 offset:1024
	ds_read_b128 v[154:157], v197 offset:1536
	s_waitcnt lgkmcnt(0)
	s_barrier
	ds_read_b128 v[178:181], v195 offset:15360
	v_mfma_f32_16x16x32_f16 v[158:161], v[34:37], v[182:185], v[158:161]
	v_mfma_f32_16x16x32_f16 v[162:165], v[38:41], v[182:185], v[162:165]
	v_mfma_f32_16x16x32_f16 v[166:169], v[42:45], v[182:185], v[166:169]
	v_mfma_f32_16x16x32_f16 v[170:173], v[46:49], v[182:185], v[170:173]
	ds_read_b128 v[182:185], v195 offset:15376
	v_mfma_f32_16x16x32_f16 v[158:161], v[50:53], v[174:177], v[158:161]
	v_mfma_f32_16x16x32_f16 v[162:165], v[54:57], v[174:177], v[162:165]
	v_mfma_f32_16x16x32_f16 v[166:169], v[58:61], v[174:177], v[166:169]
	v_mfma_f32_16x16x32_f16 v[170:173], v[62:65], v[174:177], v[170:173]
	s_cmp_ge_u32 s24, 4
	s_cbranch_scc1 .Lskipx84
	s_cmp_eq_u32 s17, 14
	s_cbranch_scc1 .Lskipx84
	global_load_dwordx4 v[186:189], v198, s[12:13]
.Lskipx84:
	s_waitcnt lgkmcnt(1)
	ds_read_b128 v[174:177], v195 offset:15392
	v_mfma_f32_16x16x32_f16 v[158:161], v[66:69], v[178:181], v[158:161]
	v_mfma_f32_16x16x32_f16 v[162:165], v[70:73], v[178:181], v[162:165]
	v_mfma_f32_16x16x32_f16 v[166:169], v[74:77], v[178:181], v[166:169]
	v_mfma_f32_16x16x32_f16 v[170:173], v[78:81], v[178:181], v[170:173]
	global_load_dwordx4 v[190:193], v199, s[8:9]
	s_waitcnt lgkmcnt(1)
	ds_read_b128 v[178:181], v195 offset:15408
	v_mfma_f32_16x16x32_f16 v[158:161], v[82:85], v[182:185], v[158:161]
	v_mfma_f32_16x16x32_f16 v[162:165], v[86:89], v[182:185], v[162:165]
	v_mfma_f32_16x16x32_f16 v[166:169], v[90:93], v[182:185], v[166:169]
	v_mfma_f32_16x16x32_f16 v[170:173], v[94:97], v[182:185], v[170:173]
	s_add_u32 s12, s12, 0x271000
	s_waitcnt lgkmcnt(1)
	ds_read_b128 v[182:185], v194 offset:16640
	v_mfma_f32_16x16x32_f16 v[158:161], v[98:101], v[174:177], v[158:161]
	v_mfma_f32_16x16x32_f16 v[162:165], v[102:105], v[174:177], v[162:165]
	v_mfma_f32_16x16x32_f16 v[166:169], v[106:109], v[174:177], v[166:169]
	v_mfma_f32_16x16x32_f16 v[170:173], v[110:113], v[174:177], v[170:173]
	s_addc_u32 s13, s13, 0
	s_waitcnt lgkmcnt(1)
	ds_read_b128 v[174:177], v194 offset:16656
	v_mfma_f32_16x16x32_f16 v[158:161], v[114:117], v[178:181], v[158:161]
	v_mfma_f32_16x16x32_f16 v[162:165], v[118:121], v[178:181], v[162:165]
	s_add_u32 s8, s8, 0x271000
	v_mfma_f32_16x16x32_f16 v[166:169], v[122:125], v[178:181], v[166:169]
	v_mfma_f32_16x16x32_f16 v[170:173], v[126:129], v[178:181], v[170:173]
	s_addc_u32 s9, s9, 0
	s_waitcnt lgkmcnt(1)
	ds_read_b128 v[178:181], v195 offset:16640
	v_mfma_f32_16x16x32_f16 v[142:145], v[2:5], v[182:185], v[142:145]
	v_mfma_f32_16x16x32_f16 v[146:149], v[6:9], v[182:185], v[146:149]
	v_mfma_f32_16x16x32_f16 v[150:153], v[10:13], v[182:185], v[150:153]
	v_mfma_f32_16x16x32_f16 v[154:157], v[14:17], v[182:185], v[154:157]
	s_waitcnt lgkmcnt(1)
	ds_read_b128 v[182:185], v195 offset:16656
	v_mfma_f32_16x16x32_f16 v[142:145], v[18:21], v[174:177], v[142:145]
	v_mfma_f32_16x16x32_f16 v[146:149], v[22:25], v[174:177], v[146:149]
	v_mfma_f32_16x16x32_f16 v[150:153], v[26:29], v[174:177], v[150:153]
	v_mfma_f32_16x16x32_f16 v[154:157], v[30:33], v[174:177], v[154:157]
	s_waitcnt lgkmcnt(1)
	ds_read_b128 v[174:177], v194 offset:16672
	v_mfma_f32_16x16x32_f16 v[142:145], v[66:69], v[178:181], v[142:145]
	v_exp_f32_e32 v158, v158
	v_exp_f32_e32 v159, v159
	v_exp_f32_e32 v162, v162
	v_mfma_f32_16x16x32_f16 v[146:149], v[70:73], v[178:181], v[146:149]
	v_exp_f32_e32 v163, v163
	v_exp_f32_e32 v166, v166
	v_exp_f32_e32 v167, v167
	v_exp_f32_e32 v170, v170
	v_mfma_f32_16x16x32_f16 v[150:153], v[74:77], v[178:181], v[150:153]
	v_exp_f32_e32 v171, v171
	v_add_f32_e32 v166, 1.0, v166
	v_add_f32_e32 v167, 1.0, v167
	v_add_f32_e32 v162, 1.0, v162
	v_mfma_f32_16x16x32_f16 v[154:157], v[78:81], v[178:181], v[154:157]
	v_add_f32_e32 v163, 1.0, v163
	v_fma_f32 v158, v158, v166, v166
	v_fma_f32 v159, v159, v167, v167
	v_rcp_f32_e32 v162, v162
	s_waitcnt lgkmcnt(1)
	ds_read_b128 v[178:181], v194 offset:16688
	v_mfma_f32_16x16x32_f16 v[142:145], v[82:85], v[182:185], v[142:145]
	v_rcp_f32_e32 v163, v163
	v_fma_f32 v166, v166, v204, s16
	v_fma_f32 v167, v167, v204, s16
	v_rcp_f32_e32 v158, v158
	v_mfma_f32_16x16x32_f16 v[146:149], v[86:89], v[182:185], v[146:149]
	v_rcp_f32_e32 v159, v159
	v_mul_f32_e32 v130, v130, v162
	v_mul_f32_e32 v131, v131, v163
	v_fma_f32 v130, v166, v158, v130
	v_mfma_f32_16x16x32_f16 v[150:153], v[90:93], v[182:185], v[150:153]
	v_fma_f32 v131, v167, v159, v131
	v_exp_f32_e32 v162, v130
	v_exp_f32_e32 v163, v131
	v_add_f32_e32 v158, 1.0, v162
	v_mfma_f32_16x16x32_f16 v[154:157], v[94:97], v[182:185], v[154:157]
	v_add_f32_e32 v159, 1.0, v163
	v_add_f32_e32 v166, -1.0, v162
	v_add_f32_e32 v167, -1.0, v163
	v_fma_f32 v170, v170, v158, v158
	s_waitcnt lgkmcnt(1)
	ds_read_b128 v[182:185], v195 offset:16672
	v_mfma_f32_16x16x32_f16 v[142:145], v[34:37], v[174:177], v[142:145]
	v_fma_f32 v171, v171, v159, v159
	v_rcp_f32_e32 v170, v170
	v_rcp_f32_e32 v171, v171
	v_mul_f32_e32 v170, v166, v170
	v_mfma_f32_16x16x32_f16 v[146:149], v[38:41], v[174:177], v[146:149]
	v_mul_f32_e32 v171, v167, v171
	v_exp_f32_e32 v160, v160
	v_exp_f32_e32 v161, v161
	v_exp_f32_e32 v164, v164
	v_mfma_f32_16x16x32_f16 v[150:153], v[42:45], v[174:177], v[150:153]
	v_exp_f32_e32 v165, v165
	v_exp_f32_e32 v168, v168
	v_exp_f32_e32 v169, v169
	v_exp_f32_e32 v172, v172
	v_mfma_f32_16x16x32_f16 v[154:157], v[46:49], v[174:177], v[154:157]
	v_exp_f32_e32 v173, v173
	v_add_f32_e32 v168, 1.0, v168
	v_add_f32_e32 v169, 1.0, v169
	v_add_f32_e32 v164, 1.0, v164
	s_waitcnt lgkmcnt(1)
	ds_read_b128 v[174:177], v195 offset:16688
	v_mfma_f32_16x16x32_f16 v[142:145], v[50:53], v[178:181], v[142:145]
	s_waitcnt vmcnt(0)
	s_cmp_ge_u32 s24, 4
	s_cbranch_scc1 .Lskips85
	ds_write_b128 v201, v[186:189] offset:15360
.Lskips85:
	ds_write_b128 v201, v[190:193] offset:1280
	v_add_f32_e32 v165, 1.0, v165
	v_fma_f32 v160, v160, v168, v168
	v_fma_f32 v161, v161, v169, v169
	v_mfma_f32_16x16x32_f16 v[146:149], v[54:57], v[178:181], v[146:149]
	v_rcp_f32_e32 v164, v164
	v_rcp_f32_e32 v165, v165
	v_fma_f32 v168, v168, v204, s16
	v_fma_f32 v169, v169, v204, s16
	v_mfma_f32_16x16x32_f16 v[150:153], v[58:61], v[178:181], v[150:153]
	v_rcp_f32_e32 v160, v160
	v_rcp_f32_e32 v161, v161
	v_mul_f32_e32 v132, v132, v164
	v_mul_f32_e32 v133, v133, v165
	v_mfma_f32_16x16x32_f16 v[154:157], v[62:65], v[178:181], v[154:157]
	v_fma_f32 v132, v168, v160, v132
	v_fma_f32 v133, v169, v161, v133
	v_exp_f32_e32 v164, v132
	v_exp_f32_e32 v165, v133
	v_add_f32_e32 v160, 1.0, v164
	s_waitcnt lgkmcnt(3)
	ds_read_b128 v[178:181], v194 offset:17920
	v_mfma_f32_16x16x32_f16 v[142:145], v[98:101], v[182:185], v[142:145]
	v_add_f32_e32 v161, 1.0, v165
	v_add_f32_e32 v168, -1.0, v164
	v_add_f32_e32 v169, -1.0, v165
	v_fma_f32 v172, v172, v160, v160
	v_mfma_f32_16x16x32_f16 v[146:149], v[102:105], v[182:185], v[146:149]
	v_fma_f32 v173, v173, v161, v161
	v_rcp_f32_e32 v172, v172
	v_rcp_f32_e32 v173, v173
	v_mul_f32_e32 v172, v168, v172
	v_mfma_f32_16x16x32_f16 v[150:153], v[106:109], v[182:185], v[150:153]
	v_mul_f32_e32 v173, v169, v173
	v_cvt_pk_f16_f32 v170, v170, v171
	v_cvt_pk_f16_f32 v171, v172, v173
	ds_write_b64 v196, v[170:171] offset:0
	v_mfma_f32_16x16x32_f16 v[154:157], v[110:113], v[182:185], v[154:157]
	ds_read_b128 v[158:161], v197 offset:0
	ds_read_b128 v[162:165], v197 offset:512
	ds_read_b128 v[166:169], v197 offset:1024
	ds_read_b128 v[170:173], v197 offset:1536
	s_waitcnt lgkmcnt(8)
	ds_read_b128 v[182:185], v194 offset:17936
	v_mfma_f32_16x16x32_f16 v[142:145], v[114:117], v[174:177], v[142:145]
	v_mfma_f32_16x16x32_f16 v[146:149], v[118:121], v[174:177], v[146:149]
	v_mfma_f32_16x16x32_f16 v[150:153], v[122:125], v[174:177], v[150:153]
	v_mfma_f32_16x16x32_f16 v[154:157], v[126:129], v[174:177], v[154:157]
	s_waitcnt lgkmcnt(6)
	ds_read_b128 v[174:177], v195 offset:17920
	s_waitcnt lgkmcnt(5)
	v_mfma_f32_16x16x32_f16 v[158:161], v[2:5], v[178:181], v[158:161]
	s_waitcnt lgkmcnt(4)
	v_mfma_f32_16x16x32_f16 v[162:165], v[6:9], v[178:181], v[162:165]
	s_waitcnt lgkmcnt(3)
	v_mfma_f32_16x16x32_f16 v[166:169], v[10:13], v[178:181], v[166:169]
	s_waitcnt lgkmcnt(2)
	v_mfma_f32_16x16x32_f16 v[170:173], v[14:17], v[178:181], v[170:173]
	s_waitcnt lgkmcnt(1)
	ds_read_b128 v[178:181], v195 offset:17936
	v_mfma_f32_16x16x32_f16 v[158:161], v[18:21], v[182:185], v[158:161]
	v_mfma_f32_16x16x32_f16 v[162:165], v[22:25], v[182:185], v[162:165]
	v_mfma_f32_16x16x32_f16 v[166:169], v[26:29], v[182:185], v[166:169]
	v_mfma_f32_16x16x32_f16 v[170:173], v[30:33], v[182:185], v[170:173]
	s_waitcnt lgkmcnt(1)
	ds_read_b128 v[182:185], v194 offset:17952
	v_mfma_f32_16x16x32_f16 v[158:161], v[66:69], v[174:177], v[158:161]
	v_exp_f32_e32 v142, v142
	v_exp_f32_e32 v143, v143
	v_exp_f32_e32 v146, v146
	v_mfma_f32_16x16x32_f16 v[162:165], v[70:73], v[174:177], v[162:165]
	v_exp_f32_e32 v147, v147
	v_exp_f32_e32 v150, v150
	v_exp_f32_e32 v151, v151
	v_exp_f32_e32 v154, v154
	v_mfma_f32_16x16x32_f16 v[166:169], v[74:77], v[174:177], v[166:169]
	v_exp_f32_e32 v155, v155
	v_add_f32_e32 v150, 1.0, v150
	v_add_f32_e32 v151, 1.0, v151
	v_add_f32_e32 v146, 1.0, v146
	v_mfma_f32_16x16x32_f16 v[170:173], v[78:81], v[174:177], v[170:173]
	v_add_f32_e32 v147, 1.0, v147
	v_fma_f32 v142, v142, v150, v150
	v_fma_f32 v143, v143, v151, v151
	v_rcp_f32_e32 v146, v146
	s_waitcnt lgkmcnt(1)
	ds_read_b128 v[174:177], v194 offset:17968
	v_mfma_f32_16x16x32_f16 v[158:161], v[82:85], v[178:181], v[158:161]
	v_rcp_f32_e32 v147, v147
	v_fma_f32 v150, v150, v204, s16
	v_fma_f32 v151, v151, v204, s16
	v_rcp_f32_e32 v142, v142
	v_mfma_f32_16x16x32_f16 v[162:165], v[86:89], v[178:181], v[162:165]
	v_rcp_f32_e32 v143, v143
	v_mul_f32_e32 v134, v134, v146
	v_mul_f32_e32 v135, v135, v147
	v_fma_f32 v134, v150, v142, v134
	v_mfma_f32_16x16x32_f16 v[166:169], v[90:93], v[178:181], v[166:169]
	v_fma_f32 v135, v151, v143, v135
	v_exp_f32_e32 v146, v134
	v_exp_f32_e32 v147, v135
	v_add_f32_e32 v142, 1.0, v146
	v_mfma_f32_16x16x32_f16 v[170:173], v[94:97], v[178:181], v[170:173]
	v_add_f32_e32 v143, 1.0, v147
	v_add_f32_e32 v150, -1.0, v146
	v_add_f32_e32 v151, -1.0, v147
	v_fma_f32 v154, v154, v142, v142
	s_waitcnt lgkmcnt(1)
	ds_read_b128 v[178:181], v195 offset:17952
	v_mfma_f32_16x16x32_f16 v[158:161], v[34:37], v[182:185], v[158:161]
	v_fma_f32 v155, v155, v143, v143
	v_rcp_f32_e32 v154, v154
	v_rcp_f32_e32 v155, v155
	v_mul_f32_e32 v154, v150, v154
	v_mfma_f32_16x16x32_f16 v[162:165], v[38:41], v[182:185], v[162:165]
	v_mul_f32_e32 v155, v151, v155
	v_exp_f32_e32 v144, v144
	v_exp_f32_e32 v145, v145
	v_exp_f32_e32 v148, v148
	v_mfma_f32_16x16x32_f16 v[166:169], v[42:45], v[182:185], v[166:169]
	v_exp_f32_e32 v149, v149
	v_exp_f32_e32 v152, v152
	v_exp_f32_e32 v153, v153
	v_exp_f32_e32 v156, v156
	v_mfma_f32_16x16x32_f16 v[170:173], v[46:49], v[182:185], v[170:173]
	v_exp_f32_e32 v157, v157
	v_add_f32_e32 v152, 1.0, v152
	v_add_f32_e32 v153, 1.0, v153
	v_add_f32_e32 v148, 1.0, v148
	s_waitcnt lgkmcnt(1)
	ds_read_b128 v[182:185], v195 offset:17968
	v_mfma_f32_16x16x32_f16 v[158:161], v[50:53], v[174:177], v[158:161]
	v_add_f32_e32 v149, 1.0, v149
	v_fma_f32 v144, v144, v152, v152
	v_fma_f32 v145, v145, v153, v153
	v_rcp_f32_e32 v148, v148
	v_mfma_f32_16x16x32_f16 v[162:165], v[54:57], v[174:177], v[162:165]
	v_rcp_f32_e32 v149, v149
	v_fma_f32 v152, v152, v204, s16
	v_fma_f32 v153, v153, v204, s16
	v_rcp_f32_e32 v144, v144
	v_mfma_f32_16x16x32_f16 v[166:169], v[58:61], v[174:177], v[166:169]
	v_rcp_f32_e32 v145, v145
	v_mul_f32_e32 v136, v136, v148
	v_mul_f32_e32 v137, v137, v149
	v_fma_f32 v136, v152, v144, v136
	v_mfma_f32_16x16x32_f16 v[170:173], v[62:65], v[174:177], v[170:173]
	v_fma_f32 v137, v153, v145, v137
	v_exp_f32_e32 v148, v136
	v_exp_f32_e32 v149, v137
	v_add_f32_e32 v144, 1.0, v148
	s_waitcnt lgkmcnt(1)
	ds_read_b128 v[174:177], v194 offset:0
	v_mfma_f32_16x16x32_f16 v[158:161], v[98:101], v[178:181], v[158:161]
	v_add_f32_e32 v145, 1.0, v149
	v_add_f32_e32 v152, -1.0, v148
	v_add_f32_e32 v153, -1.0, v149
	v_fma_f32 v156, v156, v144, v144
	v_mfma_f32_16x16x32_f16 v[162:165], v[102:105], v[178:181], v[162:165]
	v_fma_f32 v157, v157, v145, v145
	v_rcp_f32_e32 v156, v156
	v_rcp_f32_e32 v157, v157
	v_mul_f32_e32 v156, v152, v156
	v_mfma_f32_16x16x32_f16 v[166:169], v[106:109], v[178:181], v[166:169]
	v_mul_f32_e32 v157, v153, v157
	v_cvt_pk_f16_f32 v154, v154, v155
	v_cvt_pk_f16_f32 v155, v156, v157
	ds_write_b64 v196, v[154:155] offset:1280
	v_mfma_f32_16x16x32_f16 v[170:173], v[110:113], v[178:181], v[170:173]
	ds_read_b128 v[142:145], v197 offset:0
	ds_read_b128 v[146:149], v197 offset:512
	ds_read_b128 v[150:153], v197 offset:1024
	ds_read_b128 v[154:157], v197 offset:1536
	s_waitcnt lgkmcnt(6)
	ds_read_b128 v[178:181], v194 offset:16
	v_mfma_f32_16x16x32_f16 v[158:161], v[114:117], v[182:185], v[158:161]
	v_mfma_f32_16x16x32_f16 v[162:165], v[118:121], v[182:185], v[162:165]
	v_mfma_f32_16x16x32_f16 v[166:169], v[122:125], v[182:185], v[166:169]
	v_mfma_f32_16x16x32_f16 v[170:173], v[126:129], v[182:185], v[170:173]
	s_waitcnt lgkmcnt(6)
	ds_read_b128 v[182:185], v194 offset:32
	s_waitcnt lgkmcnt(5)
	v_mfma_f32_16x16x32_f16 v[142:145], v[2:5], v[174:177], v[142:145]
	s_waitcnt lgkmcnt(4)
	v_mfma_f32_16x16x32_f16 v[146:149], v[6:9], v[174:177], v[146:149]
	s_waitcnt lgkmcnt(3)
	v_mfma_f32_16x16x32_f16 v[150:153], v[10:13], v[174:177], v[150:153]
	s_waitcnt lgkmcnt(2)
	v_mfma_f32_16x16x32_f16 v[154:157], v[14:17], v[174:177], v[154:157]
	s_waitcnt lgkmcnt(1)
	ds_read_b128 v[174:177], v194 offset:48
	v_mfma_f32_16x16x32_f16 v[142:145], v[18:21], v[178:181], v[142:145]
	v_exp_f32_e32 v158, v158
	v_exp_f32_e32 v159, v159
	v_exp_f32_e32 v162, v162
	v_exp_f32_e32 v163, v163
	v_exp_f32_e32 v166, v166
	v_exp_f32_e32 v167, v167
	v_exp_f32_e32 v170, v170
	v_exp_f32_e32 v171, v171
	v_add_f32_e32 v166, 1.0, v166
	v_add_f32_e32 v167, 1.0, v167
	v_add_f32_e32 v162, 1.0, v162
	v_add_f32_e32 v163, 1.0, v163
	v_fma_f32 v158, v158, v166, v166
	v_fma_f32 v159, v159, v167, v167
	v_rcp_f32_e32 v162, v162
	v_rcp_f32_e32 v163, v163
	v_fma_f32 v166, v166, v204, s16
	v_fma_f32 v167, v167, v204, s16
	v_rcp_f32_e32 v158, v158
	v_mfma_f32_16x16x32_f16 v[146:149], v[22:25], v[178:181], v[146:149]
	v_rcp_f32_e32 v159, v159
	v_mul_f32_e32 v138, v138, v162
	v_mul_f32_e32 v139, v139, v163
	v_fma_f32 v138, v166, v158, v138
	v_fma_f32 v139, v167, v159, v139
	v_exp_f32_e32 v162, v138
	v_exp_f32_e32 v163, v139
	v_add_f32_e32 v158, 1.0, v162
	v_add_f32_e32 v159, 1.0, v163
	v_add_f32_e32 v166, -1.0, v162
	v_add_f32_e32 v167, -1.0, v163
	v_fma_f32 v170, v170, v158, v158
	v_fma_f32 v171, v171, v159, v159
	v_rcp_f32_e32 v170, v170
	v_rcp_f32_e32 v171, v171
	v_mul_f32_e32 v170, v166, v170
	v_mul_f32_e32 v171, v167, v171
	v_exp_f32_e32 v160, v160
	v_exp_f32_e32 v161, v161
	v_exp_f32_e32 v164, v164
	v_mfma_f32_16x16x32_f16 v[150:153], v[26:29], v[178:181], v[150:153]
	v_exp_f32_e32 v165, v165
	v_exp_f32_e32 v168, v168
	v_exp_f32_e32 v169, v169
	v_exp_f32_e32 v172, v172
	v_exp_f32_e32 v173, v173
	v_add_f32_e32 v168, 1.0, v168
	v_add_f32_e32 v169, 1.0, v169
	v_add_f32_e32 v164, 1.0, v164
	v_add_f32_e32 v165, 1.0, v165
	v_fma_f32 v160, v160, v168, v168
	v_fma_f32 v161, v161, v169, v169
	v_rcp_f32_e32 v164, v164
	v_rcp_f32_e32 v165, v165
	v_fma_f32 v168, v168, v204, s16
	v_fma_f32 v169, v169, v204, s16
	v_rcp_f32_e32 v160, v160
	v_rcp_f32_e32 v161, v161
	v_mul_f32_e32 v140, v140, v164
	v_mul_f32_e32 v141, v141, v165
	v_fma_f32 v140, v168, v160, v140
	v_mfma_f32_16x16x32_f16 v[154:157], v[30:33], v[178:181], v[154:157]
	v_fma_f32 v141, v169, v161, v141
	v_exp_f32_e32 v164, v140
	v_exp_f32_e32 v165, v141
	v_add_f32_e32 v160, 1.0, v164
	v_add_f32_e32 v161, 1.0, v165
	v_add_f32_e32 v168, -1.0, v164
	v_add_f32_e32 v169, -1.0, v165
	v_fma_f32 v172, v172, v160, v160
	v_fma_f32 v173, v173, v161, v161
	v_rcp_f32_e32 v172, v172
	v_rcp_f32_e32 v173, v173
	v_mul_f32_e32 v172, v168, v172
	v_mul_f32_e32 v173, v169, v173
	v_cvt_pk_f16_f32 v170, v170, v171
	v_cvt_pk_f16_f32 v171, v172, v173
	ds_write_b64 v196, v[170:171] offset:2560
	ds_read_b128 v[158:161], v197 offset:0
	ds_read_b128 v[162:165], v197 offset:512
	ds_read_b128 v[166:169], v197 offset:1024
	ds_read_b128 v[170:173], v197 offset:1536
	s_waitcnt lgkmcnt(0)
	s_barrier
	s_add_u32 s17, s17, 2
	s_cmp_lt_u32 s17, 16
	s_cbranch_scc1 .Llstm2_loop
	s_waitcnt lgkmcnt(0)
	s_load_dwordx2 s[4:5], s[0:1], 0x38
	s_load_dwordx2 s[6:7], s[0:1], 0x40
	s_load_dwordx2 s[8:9], s[0:1], 0x48
	s_load_dwordx2 s[10:11], s[0:1], 0x50
	s_load_dwordx2 s[12:13], s[0:1], 0x58
	s_load_dwordx2 s[14:15], s[0:1], 0x60
	v_and_b32_e32 v1, 15, v0
	v_bfe_u32 v205, v0, 4, 2
	v_lshrrev_b32_e32 v206, 6, v0
	s_mul_i32 s22, s2, 48
	v_lshl_add_u32 v200, v206, 2, v205
	v_lshlrev_b32_e32 v200, 4, v200
	v_add_u32_e32 v198, s22, v1
	s_waitcnt lgkmcnt(0)
	v_min_u32_e32 v199, 0x270f, v198
	v_lshl_add_u32 v199, v199, 9, v200
	global_load_dwordx4 v[142:145], v199, s[14:15]
	v_add_u32_e32 v198, 16, v198
	v_min_u32_e32 v199, 0x270f, v198
	v_lshl_add_u32 v199, v199, 9, v200
	global_load_dwordx4 v[146:149], v199, s[14:15]
	v_add_u32_e32 v198, 16, v198
	v_min_u32_e32 v199, 0x270f, v198
	v_lshl_add_u32 v199, v199, 9, v200
	global_load_dwordx4 v[150:153], v199, s[14:15]
	global_load_dwordx4 v[158:161], v200, s[6:7]
	global_load_dwordx4 v[162:165], v200, s[8:9]
	v_and_b32_e32 v1, 63, v0
	v_lshlrev_b32_e32 v1, 4, v1
	v_lshl_add_u32 v1, v206, 10, v1
	global_load_dwordx4 v[2:5], v1, s[4:5]
	v_add_u32_e32 v1, 0x2000, v1
	global_load_dwordx4 v[6:9], v1, s[4:5]
	v_add_u32_e32 v1, 0x2000, v1
	global_load_dwordx4 v[10:13], v1, s[4:5]
	v_add_u32_e32 v1, 0x2000, v1
	global_load_dwordx4 v[14:17], v1, s[4:5]
	v_add_u32_e32 v1, 0x2000, v1
	global_load_dwordx4 v[18:21], v1, s[4:5]
	v_add_u32_e32 v1, 0x2000, v1
	global_load_dwordx4 v[22:25], v1, s[4:5]
	v_add_u32_e32 v1, 0x2000, v1
	global_load_dwordx4 v[26:29], v1, s[4:5]
	v_add_u32_e32 v1, 0x2000, v1
	global_load_dwordx4 v[30:33], v1, s[4:5]
	s_waitcnt vmcnt(0)
	ds_read_b128 v[174:177], v207 offset:0
	ds_read_b128 v[178:181], v207 offset:1280
	ds_read_b128 v[182:185], v207 offset:2560
	s_waitcnt lgkmcnt(2)
	v_mfma_f32_16x16x32_f16 v[142:145], v[2:5], v[174:177], v[142:145]
	ds_read_b128 v[174:177], v207 offset:16
	s_waitcnt lgkmcnt(2)
	v_mfma_f32_16x16x32_f16 v[146:149], v[2:5], v[178:181], v[146:149]
	ds_read_b128 v[178:181], v207 offset:1296
	s_waitcnt lgkmcnt(2)
	v_mfma_f32_16x16x32_f16 v[150:153], v[2:5], v[182:185], v[150:153]
	ds_read_b128 v[182:185], v207 offset:2576
	s_waitcnt lgkmcnt(2)
	v_mfma_f32_16x16x32_f16 v[142:145], v[6:9], v[174:177], v[142:145]
	ds_read_b128 v[174:177], v207 offset:32
	s_waitcnt lgkmcnt(2)
	v_mfma_f32_16x16x32_f16 v[146:149], v[6:9], v[178:181], v[146:149]
	ds_read_b128 v[178:181], v207 offset:1312
	s_waitcnt lgkmcnt(2)
	v_mfma_f32_16x16x32_f16 v[150:153], v[6:9], v[182:185], v[150:153]
	ds_read_b128 v[182:185], v207 offset:2592
	s_waitcnt lgkmcnt(2)
	v_mfma_f32_16x16x32_f16 v[142:145], v[10:13], v[174:177], v[142:145]
	ds_read_b128 v[174:177], v207 offset:48
	s_waitcnt lgkmcnt(2)
	v_mfma_f32_16x16x32_f16 v[146:149], v[10:13], v[178:181], v[146:149]
	ds_read_b128 v[178:181], v207 offset:1328
	s_waitcnt lgkmcnt(2)
	v_mfma_f32_16x16x32_f16 v[150:153], v[10:13], v[182:185], v[150:153]
	ds_read_b128 v[182:185], v207 offset:2608
	s_waitcnt lgkmcnt(2)
	v_mfma_f32_16x16x32_f16 v[142:145], v[14:17], v[174:177], v[142:145]
	ds_read_b128 v[174:177], v195 offset:0
	s_waitcnt lgkmcnt(2)
	v_mfma_f32_16x16x32_f16 v[146:149], v[14:17], v[178:181], v[146:149]
	ds_read_b128 v[178:181], v195 offset:1280
	s_waitcnt lgkmcnt(2)
	v_mfma_f32_16x16x32_f16 v[150:153], v[14:17], v[182:185], v[150:153]
	ds_read_b128 v[182:185], v195 offset:2560
	s_waitcnt lgkmcnt(2)
	v_mfma_f32_16x16x32_f16 v[142:145], v[18:21], v[174:177], v[142:145]
	ds_read_b128 v[174:177], v195 offset:16
	s_waitcnt lgkmcnt(2)
	v_mfma_f32_16x16x32_f16 v[146:149], v[18:21], v[178:181], v[146:149]
	ds_read_b128 v[178:181], v195 offset:1296
	s_waitcnt lgkmcnt(2)
	v_mfma_f32_16x16x32_f16 v[150:153], v[18:21], v[182:185], v[150:153]
	ds_read_b128 v[182:185], v195 offset:2576
	s_waitcnt lgkmcnt(2)
	v_mfma_f32_16x16x32_f16 v[142:145], v[22:25], v[174:177], v[142:145]
	ds_read_b128 v[174:177], v195 offset:32
	s_waitcnt lgkmcnt(2)
	v_mfma_f32_16x16x32_f16 v[146:149], v[22:25], v[178:181], v[146:149]
	ds_read_b128 v[178:181], v195 offset:1312
	s_waitcnt lgkmcnt(2)
	v_mfma_f32_16x16x32_f16 v[150:153], v[22:25], v[182:185], v[150:153]
	ds_read_b128 v[182:185], v195 offset:2592
	s_waitcnt lgkmcnt(2)
	v_mfma_f32_16x16x32_f16 v[142:145], v[26:29], v[174:177], v[142:145]
	ds_read_b128 v[174:177], v195 offset:48
	s_waitcnt lgkmcnt(2)
	v_mfma_f32_16x16x32_f16 v[146:149], v[26:29], v[178:181], v[146:149]
	ds_read_b128 v[178:181], v195 offset:1328
	s_waitcnt lgkmcnt(2)
	v_mfma_f32_16x16x32_f16 v[150:153], v[26:29], v[182:185], v[150:153]
	ds_read_b128 v[182:185], v195 offset:2608
	s_waitcnt lgkmcnt(2)
	v_mfma_f32_16x16x32_f16 v[142:145], v[30:33], v[174:177], v[142:145]
	s_waitcnt lgkmcnt(1)
	v_mfma_f32_16x16x32_f16 v[146:149], v[30:33], v[178:181], v[146:149]
	s_waitcnt lgkmcnt(0)
	v_mfma_f32_16x16x32_f16 v[150:153], v[30:33], v[182:185], v[150:153]
	s_nop 7
	s_nop 1
	v_add_f32_e32 v142, v142, v158
	v_add_f32_e32 v143, v143, v159
	v_add_f32_e32 v144, v144, v160
	v_add_f32_e32 v145, v145, v161
	v_max_f32_e32 v142, 0, v142
	v_max_f32_e32 v143, 0, v143
	v_max_f32_e32 v144, 0, v144
	v_max_f32_e32 v145, 0, v145
	v_mul_f32_e32 v166, v142, v162
	v_fma_f32 v166, v143, v163, v166
	v_fma_f32 v166, v144, v164, v166
	v_fma_f32 v166, v145, v165, v166
	ds_write_b32 v208, v166 offset:0
	v_add_f32_e32 v146, v146, v158
	v_add_f32_e32 v147, v147, v159
	v_add_f32_e32 v148, v148, v160
	v_add_f32_e32 v149, v149, v161
	v_max_f32_e32 v146, 0, v146
	v_max_f32_e32 v147, 0, v147
	v_max_f32_e32 v148, 0, v148
	v_max_f32_e32 v149, 0, v149
	v_mul_f32_e32 v167, v146, v162
	v_fma_f32 v167, v147, v163, v167
	v_fma_f32 v167, v148, v164, v167
	v_fma_f32 v167, v149, v165, v167
	ds_write_b32 v208, v167 offset:2048
	v_add_f32_e32 v150, v150, v158
	v_add_f32_e32 v151, v151, v159
	v_add_f32_e32 v152, v152, v160
	v_add_f32_e32 v153, v153, v161
	v_max_f32_e32 v150, 0, v150
	v_max_f32_e32 v151, 0, v151
	v_max_f32_e32 v152, 0, v152
	v_max_f32_e32 v153, 0, v153
	v_mul_f32_e32 v168, v150, v162
	v_fma_f32 v168, v151, v163, v168
	v_fma_f32 v168, v152, v164, v168
	v_fma_f32 v168, v153, v165, v168
	ds_write_b32 v208, v168 offset:4096
	s_waitcnt lgkmcnt(0)
	s_barrier
	v_add_u32_e32 v205, s22, v0
	s_movk_i32 s23, 0x2710
	v_cmp_gt_u32_e64 s[16:17], s23, v205
	v_cmp_gt_u32_e64 s[18:19], 48, v0
	s_nop 3
	s_and_b64 s[16:17], s[16:17], s[18:19]
	s_and_saveexec_b64 s[18:19], s[16:17]
	s_cbranch_execz .Ll2_end
	v_lshlrev_b32_e32 v1, 7, v0
	v_add_u32_e32 v1, 0x13400, v1
	ds_read_b128 v[2:5], v1 offset:0
	ds_read_b128 v[6:9], v1 offset:16
	ds_read_b128 v[10:13], v1 offset:32
	ds_read_b128 v[14:17], v1 offset:48
	ds_read_b128 v[18:21], v1 offset:64
	ds_read_b128 v[22:25], v1 offset:80
	ds_read_b128 v[26:29], v1 offset:96
	ds_read_b128 v[30:33], v1 offset:112
	s_load_dword s20, s[10:11], 0x0
	s_waitcnt lgkmcnt(0)
	v_mov_b32_e32 v206, s20
	v_add_f32_e32 v206, v206, v2
	v_add_f32_e32 v206, v206, v3
	v_add_f32_e32 v206, v206, v4
	v_add_f32_e32 v206, v206, v5
	v_add_f32_e32 v206, v206, v6
	v_add_f32_e32 v206, v206, v7
	v_add_f32_e32 v206, v206, v8
	v_add_f32_e32 v206, v206, v9
	v_add_f32_e32 v206, v206, v10
	v_add_f32_e32 v206, v206, v11
	v_add_f32_e32 v206, v206, v12
	v_add_f32_e32 v206, v206, v13
	v_add_f32_e32 v206, v206, v14
	v_add_f32_e32 v206, v206, v15
	v_add_f32_e32 v206, v206, v16
	v_add_f32_e32 v206, v206, v17
	v_add_f32_e32 v206, v206, v18
	v_add_f32_e32 v206, v206, v19
	v_add_f32_e32 v206, v206, v20
	v_add_f32_e32 v206, v206, v21
	v_add_f32_e32 v206, v206, v22
	v_add_f32_e32 v206, v206, v23
	v_add_f32_e32 v206, v206, v24
	v_add_f32_e32 v206, v206, v25
	v_add_f32_e32 v206, v206, v26
	v_add_f32_e32 v206, v206, v27
	v_add_f32_e32 v206, v206, v28
	v_add_f32_e32 v206, v206, v29
	v_add_f32_e32 v206, v206, v30
	v_add_f32_e32 v206, v206, v31
	v_add_f32_e32 v206, v206, v32
	v_add_f32_e32 v206, v206, v33
	v_max_f32_e32 v206, 0, v206
	v_lshlrev_b32_e32 v205, 2, v205
	global_store_dword v205, v206, s[12:13]

amdhsa.kernels:
  - .agpr_count:     0
    .args:
      - .actual_access:  read_only
        .address_space:  global
        .offset:         0
        .size:           8
        .value_kind:     global_buffer
      - .actual_access:  read_only
        .address_space:  global
        .offset:         8
        .size:           8
        .value_kind:     global_buffer
      - .actual_access:  read_only
        .address_space:  global
        .offset:         16
        .size:           8
        .value_kind:     global_buffer
      - .actual_access:  read_only
        .address_space:  global
        .offset:         24
        .size:           8
        .value_kind:     global_buffer
      - .actual_access:  write_only
        .address_space:  global
        .offset:         32
        .size:           8
        .value_kind:     global_buffer
      - .actual_access:  write_only
        .address_space:  global
        .offset:         40
        .size:           8
        .value_kind:     global_buffer
    .group_segment_fixed_size: 56512
    .kernarg_segment_align: 8
    .kernarg_segment_size: 48
    .language:       OpenCL C
    .language_version:
      - 2
      - 0
    .max_flat_workgroup_size: 1024
    .name:           _Z10k_bscatterPKiS0_PKfS0_PiP15HIP_vector_typeIiLj2EE
    .private_segment_fixed_size: 0
    .sgpr_count:     42
    .sgpr_spill_count: 0
    .symbol:         _Z10k_bscatterPKiS0_PKfS0_PiP15HIP_vector_typeIiLj2EE.kd
    .uniform_work_group_size: 1
    .uses_dynamic_stack: false
    .vgpr_count:     89
    .vgpr_spill_count: 0
    .wavefront_size: 64
  - .agpr_count:     0
    .args:
      - .actual_access:  read_only
        .address_space:  global
        .offset:         0
        .size:           8
        .value_kind:     global_buffer
      - .actual_access:  read_only
        .address_space:  global
        .offset:         8
        .size:           8
        .value_kind:     global_buffer
      - .actual_access:  write_only
        .address_space:  global
        .offset:         16
        .size:           8
        .value_kind:     global_buffer
      - .actual_access:  write_only
        .address_space:  global
        .offset:         24
        .size:           8
        .value_kind:     global_buffer
      - .actual_access:  write_only
        .address_space:  global
        .offset:         32
        .size:           8
        .value_kind:     global_buffer
      - .actual_access:  write_only
        .address_space:  global
        .offset:         40
        .size:           8
        .value_kind:     global_buffer
      - .actual_access:  read_only
        .address_space:  global
        .offset:         48
        .size:           8
        .value_kind:     global_buffer
      - .actual_access:  write_only
        .address_space:  global
        .offset:         56
        .size:           8
        .value_kind:     global_buffer
    .group_segment_fixed_size: 12352
    .kernarg_segment_align: 8
    .kernarg_segment_size: 64
    .language:       OpenCL C
    .language_version:
      - 2
      - 0
    .max_flat_workgroup_size: 1024
    .name:           _Z8k_bfinalPK15HIP_vector_typeIiLj2EEPKiPS0_PiS6_PfPKfPDF16_
    .private_segment_fixed_size: 0
    .sgpr_count:     38
    .sgpr_spill_count: 0
    .symbol:         _Z8k_bfinalPK15HIP_vector_typeIiLj2EEPKiPS0_PiS6_PfPKfPDF16_.kd
    .uniform_work_group_size: 1
    .uses_dynamic_stack: false
    .vgpr_count:     72
    .vgpr_spill_count: 0
    .wavefront_size: 64
  - .agpr_count:     0
    .args:
      - .actual_access:  read_only
        .address_space:  global
        .offset:         0
        .size:           8
        .value_kind:     global_buffer
      - .actual_access:  write_only
        .address_space:  global
        .offset:         8
        .size:           8
        .value_kind:     global_buffer
      - .actual_access:  write_only
        .address_space:  global
        .offset:         16
        .size:           8
        .value_kind:     global_buffer
      - .actual_access:  read_only
        .address_space:  global
        .offset:         24
        .size:           8
        .value_kind:     global_buffer
      - .actual_access:  read_only
        .address_space:  global
        .offset:         32
        .size:           8
        .value_kind:     global_buffer
      - .actual_access:  write_only
        .address_space:  global
        .offset:         40
        .size:           8
        .value_kind:     global_buffer
      - .actual_access:  read_only
        .address_space:  global
        .offset:         48
        .size:           8
        .value_kind:     global_buffer
      - .actual_access:  read_only
        .address_space:  global
        .offset:         56
        .size:           8
        .value_kind:     global_buffer
      - .actual_access:  read_only
        .address_space:  global
        .offset:         64
        .size:           8
        .value_kind:     global_buffer
      - .actual_access:  read_only
        .address_space:  global
        .offset:         72
        .size:           8
        .value_kind:     global_buffer
      - .actual_access:  read_only
        .address_space:  global
        .offset:         80
        .size:           8
        .value_kind:     global_buffer
      - .actual_access:  read_only
        .address_space:  global
        .offset:         88
        .size:           8
        .value_kind:     global_buffer
      - .actual_access:  write_only
        .address_space:  global
        .offset:         96
        .size:           8
        .value_kind:     global_buffer
      - .actual_access:  write_only
        .address_space:  global
        .offset:         104
        .size:           8
        .value_kind:     global_buffer
      - .actual_access:  write_only
        .address_space:  global
        .offset:         112
        .size:           8
        .value_kind:     global_buffer
      - .actual_access:  write_only
        .address_space:  global
        .offset:         120
        .size:           8
        .value_kind:     global_buffer
      - .actual_access:  write_only
        .address_space:  global
        .offset:         128
        .size:           8
        .value_kind:     global_buffer
    .group_segment_fixed_size: 628
    .kernarg_segment_align: 8
    .kernarg_segment_size: 136
    .language:       OpenCL C
    .language_version:
      - 2
      - 0
    .max_flat_workgroup_size: 1024
    .name:           _Z7k_bhistPKiPiPfPKfS4_PDF16_S4_S4_S4_S4_S4_S4_S5_S5_S5_S5_S2_
    .private_segment_fixed_size: 0
    .sgpr_count:     25
    .sgpr_spill_count: 0
    .symbol:         _Z7k_bhistPKiPiPfPKfS4_PDF16_S4_S4_S4_S4_S4_S4_S5_S5_S5_S5_S2_.kd
    .uniform_work_group_size: 1
    .uses_dynamic_stack: false
    .vgpr_count:     32
    .vgpr_spill_count: 0
    .wavefront_size: 64
  - .agpr_count:     0
    .args:
      - .actual_access:  read_only
        .address_space:  global
        .offset:         0
        .size:           8
        .value_kind:     global_buffer
      - .actual_access:  read_only
        .address_space:  global
        .offset:         8
        .size:           8
        .value_kind:     global_buffer
      - .actual_access:  read_only
        .address_space:  global
        .offset:         16
        .size:           8
        .value_kind:     global_buffer
      - .actual_access:  read_only
        .address_space:  global
        .offset:         24
        .size:           8
        .value_kind:     global_buffer
      - .actual_access:  read_only
        .address_space:  global
        .offset:         32
        .size:           8
        .value_kind:     global_buffer
      - .actual_access:  read_only
        .address_space:  global
        .offset:         40
        .size:           8
        .value_kind:     global_buffer
      - .actual_access:  read_only
        .address_space:  global
        .offset:         48
        .size:           8
        .value_kind:     global_buffer
      - .actual_access:  read_only
        .address_space:  global
        .offset:         56
        .size:           8
        .value_kind:     global_buffer
      - .actual_access:  read_only
        .address_space:  global
        .offset:         64
        .size:           8
        .value_kind:     global_buffer
      - .actual_access:  write_only
        .address_space:  global
        .offset:         72
        .size:           8
        .value_kind:     global_buffer
      - .actual_access:  write_only
        .address_space:  global
        .offset:         80
        .size:           8
        .value_kind:     global_buffer
      - .offset:         88
        .size:           4
        .value_kind:     hidden_block_count_x
      - .offset:         92
        .size:           4
        .value_kind:     hidden_block_count_y
      - .offset:         96
        .size:           4
        .value_kind:     hidden_block_count_z
      - .offset:         100
        .size:           2
        .value_kind:     hidden_group_size_x
      - .offset:         102
        .size:           2
        .value_kind:     hidden_group_size_y
      - .offset:         104
        .size:           2
        .value_kind:     hidden_group_size_z
      - .offset:         106
        .size:           2
        .value_kind:     hidden_remainder_x
      - .offset:         108
        .size:           2
        .value_kind:     hidden_remainder_y
      - .offset:         110
        .size:           2
        .value_kind:     hidden_remainder_z
      - .offset:         128
        .size:           8
        .value_kind:     hidden_global_offset_x
      - .offset:         136
        .size:           8
        .value_kind:     hidden_global_offset_y
      - .offset:         144
        .size:           8
        .value_kind:     hidden_global_offset_z
      - .offset:         152
        .size:           2
        .value_kind:     hidden_grid_dims
    .group_segment_fixed_size: 2048
    .kernarg_segment_align: 8
    .kernarg_segment_size: 344
    .language:       OpenCL C
    .language_version:
      - 2
      - 0
    .max_flat_workgroup_size: 256
    .name:           _Z7k_fold2PKfS0_S0_S0_S0_S0_S0_S0_S0_PDF16_Pf
    .private_segment_fixed_size: 0
    .sgpr_count:     36
    .sgpr_spill_count: 0
    .symbol:         _Z7k_fold2PKfS0_S0_S0_S0_S0_S0_S0_S0_PDF16_Pf.kd
    .uniform_work_group_size: 1
    .uses_dynamic_stack: false
    .vgpr_count:     61
    .vgpr_spill_count: 0
    .wavefront_size: 64
  - .agpr_count:     0
    .args:
      - .actual_access:  read_only
        .address_space:  global
        .offset:         0
        .size:           8
        .value_kind:     global_buffer
      - .actual_access:  read_only
        .address_space:  global
        .offset:         8
        .size:           8
        .value_kind:     global_buffer
      - .actual_access:  write_only
        .address_space:  global
        .offset:         16
        .size:           8
        .value_kind:     global_buffer
      - .actual_access:  read_only
        .address_space:  global
        .offset:         24
        .size:           8
        .value_kind:     global_buffer
      - .actual_access:  read_only
        .address_space:  global
        .offset:         32
        .size:           8
        .value_kind:     global_buffer
      - .actual_access:  read_only
        .address_space:  global
        .offset:         40
        .size:           8
        .value_kind:     global_buffer
      - .actual_access:  read_only
        .address_space:  global
        .offset:         48
        .size:           8
        .value_kind:     global_buffer
      - .actual_access:  read_only
        .address_space:  global
        .offset:         56
        .size:           8
        .value_kind:     global_buffer
      - .actual_access:  read_only
        .address_space:  global
        .offset:         64
        .size:           8
        .value_kind:     global_buffer
      - .actual_access:  read_only
        .address_space:  global
        .offset:         72
        .size:           8
        .value_kind:     global_buffer
      - .actual_access:  read_only
        .address_space:  global
        .offset:         80
        .size:           8
        .value_kind:     global_buffer
      - .actual_access:  write_only
        .address_space:  global
        .offset:         88
        .size:           8
        .value_kind:     global_buffer
      - .actual_access:  write_only
        .address_space:  global
        .offset:         96
        .size:           8
        .value_kind:     global_buffer
      - .address_space:  global
        .offset:         104
        .size:           8
        .value_kind:     global_buffer
      - .actual_access:  write_only
        .address_space:  global
        .offset:         112
        .size:           8
        .value_kind:     global_buffer
      - .actual_access:  read_only
        .address_space:  global
        .offset:         120
        .size:           8
        .value_kind:     global_buffer
      - .actual_access:  read_only
        .address_space:  global
        .offset:         128
        .size:           8
        .value_kind:     global_buffer
    .group_segment_fixed_size: 22272
    .kernarg_segment_align: 8
    .kernarg_segment_size: 136
    .language:       OpenCL C
    .language_version:
      - 2
      - 0
    .max_flat_workgroup_size: 256
    .name:           _Z5k_gcnILi1EEvPKvPK15HIP_vector_typeIiLj2EEPfPKiS8_PKfPKDF16_SA_SA_SA_SA_S6_PDF16_S6_SD_SC_SA_
    .private_segment_fixed_size: 0
    .sgpr_count:     35
    .sgpr_spill_count: 0
    .symbol:         _Z5k_gcnILi1EEvPKvPK15HIP_vector_typeIiLj2EEPfPKiS8_PKfPKDF16_SA_SA_SA_SA_S6_PDF16_S6_SD_SC_SA_.kd
    .uniform_work_group_size: 1
    .uses_dynamic_stack: false
    .vgpr_count:     58
    .vgpr_spill_count: 0
    .wavefront_size: 64
  - .agpr_count:     0
    .args:
      - .actual_access:  read_only
        .address_space:  global
        .offset:         0
        .size:           8
        .value_kind:     global_buffer
      - .actual_access:  read_only
        .address_space:  global
        .offset:         8
        .size:           8
        .value_kind:     global_buffer
      - .actual_access:  read_only
        .address_space:  global
        .offset:         16
        .size:           8
        .value_kind:     global_buffer
      - .actual_access:  read_only
        .address_space:  global
        .offset:         24
        .size:           8
        .value_kind:     global_buffer
      - .actual_access:  read_only
        .address_space:  global
        .offset:         32
        .size:           8
        .value_kind:     global_buffer
      - .actual_access:  read_only
        .address_space:  global
        .offset:         40
        .size:           8
        .value_kind:     global_buffer
      - .actual_access:  read_only
        .address_space:  global
        .offset:         48
        .size:           8
        .value_kind:     global_buffer
      - .actual_access:  read_only
        .address_space:  global
        .offset:         56
        .size:           8
        .value_kind:     global_buffer
      - .actual_access:  read_only
        .address_space:  global
        .offset:         64
        .size:           8
        .value_kind:     global_buffer
      - .actual_access:  read_only
        .address_space:  global
        .offset:         72
        .size:           8
        .value_kind:     global_buffer
      - .actual_access:  read_only
        .address_space:  global
        .offset:         80
        .size:           8
        .value_kind:     global_buffer
      - .actual_access:  read_only
        .address_space:  global
        .offset:         88
        .size:           8
        .value_kind:     global_buffer
      - .actual_access:  write_only
        .address_space:  global
        .offset:         96
        .size:           8
        .value_kind:     global_buffer
      - .address_space:  global
        .offset:         104
        .size:           8
        .value_kind:     global_buffer
      - .actual_access:  read_only
        .address_space:  global
        .offset:         112
        .size:           8
        .value_kind:     global_buffer
      - .actual_access:  read_only
        .address_space:  global
        .offset:         120
        .size:           8
        .value_kind:     global_buffer
      - .actual_access:  read_only
        .address_space:  global
        .offset:         128
        .size:           8
        .value_kind:     global_buffer
      - .offset:         136
        .size:           4
        .value_kind:     hidden_block_count_x
      - .offset:         140
        .size:           4
        .value_kind:     hidden_block_count_y
      - .offset:         144
        .size:           4
        .value_kind:     hidden_block_count_z
      - .offset:         148
        .size:           2
        .value_kind:     hidden_group_size_x
      - .offset:         150
        .size:           2
        .value_kind:     hidden_group_size_y
      - .offset:         152
        .size:           2
        .value_kind:     hidden_group_size_z
      - .offset:         154
        .size:           2
        .value_kind:     hidden_remainder_x
      - .offset:         156
        .size:           2
        .value_kind:     hidden_remainder_y
      - .offset:         158
        .size:           2
        .value_kind:     hidden_remainder_z
      - .offset:         176
        .size:           8
        .value_kind:     hidden_global_offset_x
      - .offset:         184
        .size:           8
        .value_kind:     hidden_global_offset_y
      - .offset:         192
        .size:           8
        .value_kind:     hidden_global_offset_z
      - .offset:         200
        .size:           2
        .value_kind:     hidden_grid_dims
    .group_segment_fixed_size: 23808
    .kernarg_segment_align: 8
    .kernarg_segment_size: 392
    .language:       OpenCL C
    .language_version:
      - 2
      - 0
    .max_flat_workgroup_size: 256
    .name:           _Z5k_gcnILi2EEvPKvPK15HIP_vector_typeIiLj2EEPfPKiS8_PKfPKDF16_SA_SA_SA_SA_S6_PDF16_S6_SD_SC_SA_
    .private_segment_fixed_size: 0
    .sgpr_count:     36
    .sgpr_spill_count: 0
    .symbol:         _Z5k_gcnILi2EEvPKvPK15HIP_vector_typeIiLj2EEPfPKiS8_PKfPKDF16_SA_SA_SA_SA_S6_PDF16_S6_SD_SC_SA_.kd
    .uniform_work_group_size: 1
    .uses_dynamic_stack: false
    .vgpr_count:     121
    .vgpr_spill_count: 0
    .wavefront_size: 64
  - .agpr_count:     0
    .args:
      - .actual_access:  read_only
        .address_space:  global
        .offset:         0
        .size:           8
        .value_kind:     global_buffer
      - .actual_access:  read_only
        .address_space:  global
        .offset:         8
        .size:           8
        .value_kind:     global_buffer
      - .actual_access:  read_only
        .address_space:  global
        .offset:         16
        .size:           8
        .value_kind:     global_buffer
      - .actual_access:  read_only
        .address_space:  global
        .offset:         24
        .size:           8
        .value_kind:     global_buffer
      - .actual_access:  write_only
        .address_space:  global
        .offset:         32
        .size:           8
        .value_kind:     global_buffer
      - .actual_access:  read_only
        .address_space:  global
        .offset:         40
        .size:           8
        .value_kind:     global_buffer
      - .actual_access:  read_only
        .address_space:  global
        .offset:         48
        .size:           8
        .value_kind:     global_buffer
      - .actual_access:  read_only
        .address_space:  global
        .offset:         56
        .size:           8
        .value_kind:     global_buffer
      - .actual_access:  read_only
        .address_space:  global
        .offset:         64
        .size:           8
        .value_kind:     global_buffer
      - .actual_access:  read_only
        .address_space:  global
        .offset:         72
        .size:           8
        .value_kind:     global_buffer
      - .actual_access:  read_only
        .address_space:  global
        .offset:         80
        .size:           8
        .value_kind:     global_buffer
      - .actual_access:  read_only
        .address_space:  global
        .offset:         88
        .size:           8
        .value_kind:     global_buffer
      - .actual_access:  write_only
        .address_space:  global
        .offset:         96
        .size:           8
        .value_kind:     global_buffer
    .group_segment_fixed_size: 9216
    .kernarg_segment_align: 8
    .kernarg_segment_size: 104
    .language:       OpenCL C
    .language_version:
      - 2
      - 0
    .max_flat_workgroup_size: 512
    .name:           _Z6k_lstmILi256ELi10ELb1ELb0EEvPKDF16_S1_S1_PKfPDF16_S1_S1_S1_S3_S3_S3_PfS5_
    .private_segment_fixed_size: 0
    .sgpr_count:     37
    .sgpr_spill_count: 0
    .symbol:         _Z6k_lstmILi256ELi10ELb1ELb0EEvPKDF16_S1_S1_PKfPDF16_S1_S1_S1_S3_S3_S3_PfS5_.kd
    .uniform_work_group_size: 1
    .uses_dynamic_stack: false
    .vgpr_count:     256
    .vgpr_spill_count: 0
    .wavefront_size: 64
  - .agpr_count:     0
    .args:
      - .actual_access:  read_only
        .address_space:  global
        .offset:         0
        .size:           8
        .value_kind:     global_buffer
      - .actual_access:  read_only
        .address_space:  global
        .offset:         8
        .size:           8
        .value_kind:     global_buffer
      - .actual_access:  read_only
        .address_space:  global
        .offset:         16
        .size:           8
        .value_kind:     global_buffer
      - .actual_access:  read_only
        .address_space:  global
        .offset:         24
        .size:           8
        .value_kind:     global_buffer
      - .actual_access:  read_only
        .address_space:  global
        .offset:         32
        .size:           8
        .value_kind:     global_buffer
      - .actual_access:  read_only
        .address_space:  global
        .offset:         40
        .size:           8
        .value_kind:     global_buffer
      - .actual_access:  read_only
        .address_space:  global
        .offset:         48
        .size:           8
        .value_kind:     global_buffer
      - .actual_access:  read_only
        .address_space:  global
        .offset:         56
        .size:           8
        .value_kind:     global_buffer
      - .actual_access:  read_only
        .address_space:  global
        .offset:         64
        .size:           8
        .value_kind:     global_buffer
      - .actual_access:  read_only
        .address_space:  global
        .offset:         72
        .size:           8
        .value_kind:     global_buffer
      - .actual_access:  read_only
        .address_space:  global
        .offset:         80
        .size:           8
        .value_kind:     global_buffer
      - .actual_access:  write_only
        .address_space:  global
        .offset:         88
        .size:           8
        .value_kind:     global_buffer
      - .actual_access:  read_only
        .address_space:  global
        .offset:         96
        .size:           8
        .value_kind:     global_buffer
    .group_segment_fixed_size: 0
    .kernarg_segment_align: 8
    .kernarg_segment_size: 104
    .language:       OpenCL C
    .language_version:
      - 2
      - 0
    .max_flat_workgroup_size: 512
    .name:           _Z6k_lstmILi128ELi8ELb0ELb1EEvPKDF16_S1_S1_PKfPDF16_S1_S1_S1_S3_S3_S3_PfS5_
    .private_segment_fixed_size: 0
    .sgpr_count:     42
    .sgpr_spill_count: 0
    .symbol:         _Z6k_lstmILi128ELi8ELb0ELb1EEvPKDF16_S1_S1_PKfPDF16_S1_S1_S1_S3_S3_S3_PfS5_.kd
    .uniform_work_group_size: 1
    .uses_dynamic_stack: false
    .vgpr_count:     224
    .vgpr_spill_count: 0
    .wavefront_size: 64
